# baseline (speedup 1.0000x reference)
.LBB1_7:
	s_or_b64 exec, exec, s[2:3]
	v_mov_b32_e32 v10, v167
	s_waitcnt lgkmcnt(0)
	s_barrier
	s_waitcnt vmcnt(18)
	v_lshrrev_b32_e32 v182, 5, v167
	s_lshr_b32 s38, s4, 1
	v_and_b32_e32 v26, 31, v167
	v_and_b32_e32 v27, 3, v167
	v_bfe_u32 v28, v167, 3, 1
	v_bfe_u32 v29, v167, 2, 1
	v_lshl_or_b32 v27, v28, 2, v27
	v_lshl_or_b32 v27, v29, 3, v27
	v_lshlrev_b32_e32 v32, 9, v182
	v_lshl_add_u32 v30, v27, 3, v32
	v_add_u32_e32 v30, 0x10000, v30
	v_lshl_add_u32 v31, v26, 3, v32
	v_add_u32_e32 v31, 0x10400, v31
	v_xor_b32_e32 v28, 31, v26
	v_lshl_add_u32 v28, v28, 3, v32
	v_add_u32_e32 v28, 0x10400, v28
	v_bfe_u32 v29, v167, 4, 1
	v_mul_u32_u24_e32 v29, 0x78, v29
	v_xor_b32_e32 v254, s38, v29
	v_or_b32_e32 v254, 0x10800, v254
	v_and_b32_e32 v33, 16, v167
	v_cmp_eq_u32_e32 vcc, 0, v33
	ds_read2_b64 v[66:69], v30 offset0:0 offset1:32
	ds_read2_b64 v[70:73], v30 offset0:16 offset1:48
	ds_read2_b64 v[230:233], v31 offset0:0 offset1:32
	ds_read2_b64 v[234:237], v28 offset0:0 offset1:32
	ds_read2_b64 v[238:241], v254 offset0:0 offset1:16
	ds_read2_b64 v[242:245], v254 offset0:32 offset1:48
	s_waitcnt lgkmcnt(0)
	v_cndmask_b32_e32 v74, v67, v66, vcc
	v_cndmask_b32_e32 v75, v69, v68, vcc
	v_cndmask_b32_e64 v76, v66, -v67, vcc
	v_cndmask_b32_e64 v77, v68, -v69, vcc
	v_cndmask_b32_e32 v78, v71, v70, vcc
	v_cndmask_b32_e32 v79, v73, v72, vcc
	v_cndmask_b32_e64 v80, v70, -v71, vcc
	v_cndmask_b32_e64 v81, v72, -v73, vcc
	v_cvt_pk_f16_f32 v222, v74, v75
	v_cvt_pk_f16_f32 v223, v74, v75
	v_cvt_pk_f16_f32 v224, v76, v77
	v_cvt_pk_f16_f32 v225, v76, v77
	v_cvt_pk_f16_f32 v226, v78, v79
	v_cvt_pk_f16_f32 v227, v78, v79
	v_cvt_pk_f16_f32 v228, v80, v81
	v_cvt_pk_f16_f32 v229, v80, v81
	v_mul_f32_e32 v66, v231, v239
	v_mul_f32_e32 v68, v231, v238
	v_mul_f32_e32 v67, v231, v241
	v_mul_f32_e32 v69, v231, v240
	v_fma_f32 v66, v230, v238, -v66
	v_fma_f32 v68, v230, v239, v68
	v_fma_f32 v67, v230, v240, -v67
	v_fma_f32 v69, v230, v241, v69
	v_cvt_pk_f16_f32 v246, v66, v67
	v_cvt_pk_f16_f32 v248, v68, v69
	v_mul_f32_e32 v70, v233, v243
	v_mul_f32_e32 v72, v233, v242
	v_mul_f32_e32 v71, v233, v245
	v_mul_f32_e32 v73, v233, v244
	v_fma_f32 v70, v232, v242, -v70
	v_fma_f32 v72, v232, v243, v72
	v_fma_f32 v71, v232, v244, -v71
	v_fma_f32 v73, v232, v245, v73
	v_cvt_pk_f16_f32 v247, v70, v71
	v_cvt_pk_f16_f32 v249, v72, v73
	v_mul_f32_e32 v66, v235, v239
	v_mul_f32_e32 v68, v235, v238
	v_mul_f32_e32 v67, v235, v241
	v_mul_f32_e32 v69, v235, v240
	v_fma_f32 v66, v234, v238, -v66
	v_fma_f32 v68, v234, v239, v68
	v_fma_f32 v67, v234, v240, -v67
	v_fma_f32 v69, v234, v241, v69
	v_cvt_pk_f16_f32 v250, v66, v67
	v_cvt_pk_f16_f32 v252, v68, v69
	v_mul_f32_e32 v70, v237, v243
	v_mul_f32_e32 v72, v237, v242
	v_mul_f32_e32 v71, v237, v245
	v_mul_f32_e32 v73, v237, v244
	v_fma_f32 v70, v236, v242, -v70
	v_fma_f32 v72, v236, v243, v72
	v_fma_f32 v71, v236, v244, -v71
	v_fma_f32 v73, v236, v245, v73
	v_cvt_pk_f16_f32 v251, v70, v71
	v_cvt_pk_f16_f32 v253, v72, v73
	v_xor_b32_e32 v255, 8, v254
	ds_read2_b64 v[238:241], v255 offset0:0 offset1:16
	ds_read2_b64 v[242:245], v255 offset0:32 offset1:48
	v_mfma_f32_32x32x16_f16 v[2:17], v[222:225], v[246:249], 0
	v_mfma_f32_32x32x16_f16 v[18:33], v[226:229], v[250:253], 0
	s_waitcnt lgkmcnt(0)
	v_mul_f32_e32 v66, v231, v239
	v_mul_f32_e32 v68, v231, v238
	v_mul_f32_e32 v67, v231, v241
	v_mul_f32_e32 v69, v231, v240
	v_fma_f32 v66, v230, v238, -v66
	v_fma_f32 v68, v230, v239, v68
	v_fma_f32 v67, v230, v240, -v67
	v_fma_f32 v69, v230, v241, v69
	v_cvt_pk_f16_f32 v246, v66, v67
	v_cvt_pk_f16_f32 v248, v68, v69
	v_mul_f32_e32 v70, v233, v243
	v_mul_f32_e32 v72, v233, v242
	v_mul_f32_e32 v71, v233, v245
	v_mul_f32_e32 v73, v233, v244
	v_fma_f32 v70, v232, v242, -v70
	v_fma_f32 v72, v232, v243, v72
	v_fma_f32 v71, v232, v244, -v71
	v_fma_f32 v73, v232, v245, v73
	v_cvt_pk_f16_f32 v247, v70, v71
	v_cvt_pk_f16_f32 v249, v72, v73
	v_cvt_pk_f16_f32 v2, v2, v3
	v_cvt_pk_f16_f32 v3, v4, v5
	v_cvt_pk_f16_f32 v4, v6, v7
	v_cvt_pk_f16_f32 v5, v8, v9
	v_cvt_pk_f16_f32 v6, v10, v11
	v_cvt_pk_f16_f32 v7, v12, v13
	v_cvt_pk_f16_f32 v8, v14, v15
	v_cvt_pk_f16_f32 v9, v16, v17
	v_cvt_pk_f16_f32 v18, v18, v19
	v_cvt_pk_f16_f32 v19, v20, v21
	v_cvt_pk_f16_f32 v20, v22, v23
	v_cvt_pk_f16_f32 v21, v24, v25
	v_cvt_pk_f16_f32 v22, v26, v27
	v_cvt_pk_f16_f32 v23, v28, v29
	v_cvt_pk_f16_f32 v24, v30, v31
	v_cvt_pk_f16_f32 v25, v32, v33
	s_setprio 1
	s_waitcnt vmcnt(14)
	s_ashr_i32 s2, s4, 6
	s_lshl_b32 s3, s2, 3
	s_and_b32 s5, s3, 8
	s_bfe_u32 s26, s2, 0x10001
	s_or_b32 s5, s26, s5
	v_mfma_f32_32x32x16_f16 v[34:49], v[2:5], v[150:153], 0
	s_lshl_b32 s26, s2, 9
	s_and_b32 s26, s26, 0x400
	s_lshl_b32 s5, s5, 4
	s_or_b32 s28, s5, s26
	v_bfe_u32 v76, v156, 4, 1
	v_mfma_f32_32x32x16_f16 v[34:49], v[18:21], v[146:149], v[34:49]
	v_bitop3_b32 v77, v182, v156, 1 bitop3:0x78
	v_lshlrev_b32_e32 v154, 2, v182
	v_xor_b32_e32 v77, v77, v76
	v_bitop3_b32 v78, v154, v156, 4 bitop3:0x78
	v_and_b32_e32 v79, 10, v156
	v_or3_b32 v77, v79, v78, v77
	v_mfma_f32_32x32x16_f16 v[34:49], v[6:9], v[142:145], v[34:49]
	s_lshl_b32 s5, s2, 4
	v_lshlrev_b32_e32 v77, 4, v77
	s_lshl_b32 s3, s2, 13
	s_and_b32 s29, s5, 16
	v_lshlrev_b32_e32 v170, 8, v182
	v_mfma_f32_32x32x16_f16 v[34:49], v[22:25], v[138:141], v[34:49]
	v_lshl_or_b32 v171, v76, 10, v77
	s_or_b32 s26, s29, s3
	v_bitop3_b32 v179, v171, s26, v170 bitop3:0x36
	s_or_b32 s5, s26, 0x280
	v_bitop3_b32 v178, v171, s5, v170 bitop3:0x36
	s_or_b32 s30, s3, 0x800
	s_waitcnt vmcnt(5)
	s_or_b32 s33, s3, 0x1000
	s_or_b32 s29, s29, 64
	s_or_b32 s34, s29, s33
	v_bitop3_b32 v180, v171, s34, v170 bitop3:0x36
	s_or_b32 s29, s3, s29
	v_mfma_f32_32x32x16_f16 v[50:65], v[2:5], v[134:137], 0
	s_or_b32 s29, s29, 0x1280
	s_and_b32 s5, s2, 1
	v_mul_f32_e32 v66, v235, v239
	v_mul_f32_e32 v68, v235, v238
	v_mul_f32_e32 v67, v235, v241
	v_mfma_f32_32x32x16_f16 v[50:65], v[18:21], v[126:129], v[50:65]
	v_mul_f32_e32 v69, v235, v240
	v_fma_f32 v66, v234, v238, -v66
	v_fma_f32 v68, v234, v239, v68
	v_fma_f32 v67, v234, v240, -v67
	v_fma_f32 v69, v234, v241, v69
	v_cvt_pk_f16_f32 v250, v66, v67
	v_mfma_f32_32x32x16_f16 v[50:65], v[6:9], v[122:125], v[50:65]
	v_cvt_pk_f16_f32 v252, v68, v69
	v_mul_f32_e32 v70, v237, v243
	v_mul_f32_e32 v72, v237, v242
	v_mul_f32_e32 v71, v237, v245
	v_mul_f32_e32 v73, v237, v244
	v_mfma_f32_32x32x16_f16 v[50:65], v[22:25], v[130:133], v[50:65]
	v_fma_f32 v70, v236, v242, -v70
	v_fma_f32 v72, v236, v243, v72
	v_fma_f32 v71, v236, v244, -v71
	v_fma_f32 v73, v236, v245, v73
	v_cvt_pk_f16_f32 v251, v70, v71
	v_cvt_pk_f16_f32 v253, v72, v73
	v_xor_b32_e32 v255, 16, v254
	ds_read2_b64 v[238:241], v255 offset0:0 offset1:16
	ds_read2_b64 v[242:245], v255 offset0:32 offset1:48
	v_mfma_f32_32x32x16_f16 v[2:17], v[222:225], v[246:249], 0
	v_mfma_f32_32x32x16_f16 v[18:33], v[226:229], v[250:253], 0
	v_cvt_pk_f16_f32 v34, v34, v35
	v_cvt_pk_f16_f32 v35, v36, v37
	v_cvt_pk_f16_f32 v36, v38, v39
	v_cvt_pk_f16_f32 v37, v40, v41
	v_cvt_pk_f16_f32 v38, v42, v43
	v_cvt_pk_f16_f32 v39, v44, v45
	v_cvt_pk_f16_f32 v40, v46, v47
	v_cvt_pk_f16_f32 v41, v48, v49
	v_cvt_pk_f16_f32 v50, v50, v51
	v_cvt_pk_f16_f32 v51, v52, v53
	v_cvt_pk_f16_f32 v52, v54, v55
	v_cvt_pk_f16_f32 v53, v56, v57
	v_cvt_pk_f16_f32 v54, v58, v59
	v_cvt_pk_f16_f32 v55, v60, v61
	v_cvt_pk_f16_f32 v56, v62, v63
	v_cvt_pk_f16_f32 v57, v64, v65
	s_waitcnt vmcnt(2)
	s_lshl_b32 s31, s5, 4
	s_or_b32 s2, s31, s3
	v_bitop3_b32 v173, v171, s2, v170 bitop3:0x36
	v_bitop3_b32 v76, v156, 31, v156 bitop3:0xc
	v_lshrrev_b32_e32 v77, 4, v76
	v_bitop3_b32 v78, v76, v182, 1 bitop3:0x6c
	v_mfma_f32_32x32x16_f16 v[190:205], v[34:37], v[118:121], 0
	v_xor_b32_e32 v78, v78, v77
	v_bitop3_b32 v76, v76, v154, 4 bitop3:0x6c
	v_bitop3_b32 v79, v156, 10, 31 bitop3:8
	v_or3_b32 v76, v79, v76, v78
	v_lshlrev_b32_e32 v77, 10, v77
	v_lshlrev_b32_e32 v76, 4, v76
	v_mfma_f32_32x32x16_f16 v[206:221], v[34:37], v[102:105], 0
	v_or3_b32 v154, v77, v76, v170
	v_bitop3_b32 v172, s2, v154, v159 bitop3:0x36
	v_bitop3_b32 v176, v171, s29, v170 bitop3:0x36
	s_or_b32 s29, s31, s30
	s_or_b32 s29, s29, 0xa0
	v_cvt_pk_f16_f32 v2, v2, v3
	v_mfma_f32_32x32x16_f16 v[190:205], v[38:41], v[114:117], v[190:205]
	v_cvt_pk_f16_f32 v3, v4, v5
	v_cvt_pk_f16_f32 v4, v6, v7
	v_cvt_pk_f16_f32 v5, v8, v9
	v_cvt_pk_f16_f32 v6, v10, v11
	v_cvt_pk_f16_f32 v7, v12, v13
	v_cvt_pk_f16_f32 v8, v14, v15
	v_mfma_f32_32x32x16_f16 v[206:221], v[38:41], v[98:101], v[206:221]
	v_cvt_pk_f16_f32 v9, v16, v17
	v_cvt_pk_f16_f32 v18, v18, v19
	v_cvt_pk_f16_f32 v19, v20, v21
	v_cvt_pk_f16_f32 v20, v22, v23
	v_cvt_pk_f16_f32 v21, v24, v25
	v_cvt_pk_f16_f32 v22, v26, v27
	v_mfma_f32_32x32x16_f16 v[190:205], v[50:53], v[110:113], v[190:205]
	v_cvt_pk_f16_f32 v23, v28, v29
	v_cvt_pk_f16_f32 v24, v30, v31
	v_cvt_pk_f16_f32 v25, v32, v33
	s_waitcnt lgkmcnt(0)
	v_mul_f32_e32 v66, v231, v239
	v_mul_f32_e32 v68, v231, v238
	v_mfma_f32_32x32x16_f16 v[206:221], v[50:53], v[94:97], v[206:221]
	v_mul_f32_e32 v67, v231, v241
	v_mul_f32_e32 v69, v231, v240
	v_fma_f32 v66, v230, v238, -v66
	v_fma_f32 v68, v230, v239, v68
	v_fma_f32 v67, v230, v240, -v67
	v_fma_f32 v69, v230, v241, v69
	v_mfma_f32_32x32x16_f16 v[190:205], v[54:57], v[106:109], v[190:205]
	v_cvt_pk_f16_f32 v246, v66, v67
	v_cvt_pk_f16_f32 v248, v68, v69
	v_mul_f32_e32 v70, v233, v243
	v_mul_f32_e32 v72, v233, v242
	v_mul_f32_e32 v71, v233, v245
	v_mul_f32_e32 v73, v233, v244
	v_mfma_f32_32x32x16_f16 v[206:221], v[54:57], v[90:93], v[206:221]
	v_fma_f32 v70, v232, v242, -v70
	v_fma_f32 v72, v232, v243, v72
	v_fma_f32 v71, v232, v244, -v71
	v_fma_f32 v73, v232, v245, v73
	v_cvt_pk_f16_f32 v247, v70, v71
	v_cvt_pk_f16_f32 v249, v72, v73
	v_mfma_f32_32x32x16_f16 v[34:49], v[2:5], v[150:153], 0
	v_bitop3_b32 v175, v171, s29, v170 bitop3:0x36
	s_or_b32 s29, s2, 0xaa0
	s_xor_b32 s29, s29, 0x80
	v_xor_b32_e32 v174, s29, v154
	s_or_b32 s29, s26, 0x18e0
	v_bitop3_b32 v181, v171, s29, v170 bitop3:0x36
	s_or_b32 s29, s26, 0x1a60
	v_mfma_f32_32x32x16_f16 v[34:49], v[18:21], v[146:149], v[34:49]
	v_bitop3_b32 v177, v171, s29, v170 bitop3:0x36
	s_or_b32 s29, s31, 64
	s_or_b32 s3, s3, s29
	s_mov_b32 s41, s3
	s_or_b32 s29, s29, s33
	s_mov_b32 s40, s29
	s_or_b32 s3, s2, 0x18e0
	v_mfma_f32_32x32x16_f16 v[34:49], v[6:9], v[142:145], v[34:49]
	s_mov_b32 s42, s3
	s_or_b32 s2, s2, 0x1ae0
	s_xor_b32 s2, s2, 0x80
	s_mov_b32 s43, s2
	v_mul_f32_e32 v66, v235, v239
	v_mul_f32_e32 v68, v235, v238
	v_mul_f32_e32 v67, v235, v241
	v_mfma_f32_32x32x16_f16 v[34:49], v[22:25], v[138:141], v[34:49]
	v_mul_f32_e32 v69, v235, v240
	v_fma_f32 v66, v234, v238, -v66
	v_fma_f32 v68, v234, v239, v68
	v_fma_f32 v67, v234, v240, -v67
	v_fma_f32 v69, v234, v241, v69
	v_cvt_pk_f16_f32 v250, v66, v67
	v_cvt_pk_f16_f32 v252, v68, v69
	v_mul_f32_e32 v70, v237, v243
	v_mfma_f32_32x32x16_f16 v[50:65], v[2:5], v[134:137], 0
	v_mul_f32_e32 v72, v237, v242
	v_mul_f32_e32 v71, v237, v245
	v_mul_f32_e32 v73, v237, v244
	v_fma_f32 v70, v236, v242, -v70
	v_fma_f32 v72, v236, v243, v72
	v_fma_f32 v71, v236, v244, -v71
	v_fma_f32 v73, v236, v245, v73
	v_mfma_f32_32x32x16_f16 v[50:65], v[18:21], v[126:129], v[50:65]
	v_cvt_pk_f16_f32 v251, v70, v71
	v_cvt_pk_f16_f32 v253, v72, v73
	v_cvt_pk_f16_f32 v190, v190, v191
	v_cvt_pk_f16_f32 v191, v192, v193
	v_cvt_pk_f16_f32 v192, v194, v195
	v_cvt_pk_f16_f32 v193, v196, v197
	v_cvt_pk_f16_f32 v194, v198, v199
	v_mfma_f32_32x32x16_f16 v[50:65], v[6:9], v[122:125], v[50:65]
	v_cvt_pk_f16_f32 v195, v200, v201
	v_cvt_pk_f16_f32 v196, v202, v203
	v_cvt_pk_f16_f32 v197, v204, v205
	v_cvt_pk_f16_f32 v206, v206, v207
	v_cvt_pk_f16_f32 v207, v208, v209
	v_cvt_pk_f16_f32 v208, v210, v211
	v_cvt_pk_f16_f32 v209, v212, v213
	v_mfma_f32_32x32x16_f16 v[50:65], v[22:25], v[130:133], v[50:65]
	v_cvt_pk_f16_f32 v210, v214, v215
	v_cvt_pk_f16_f32 v211, v216, v217
	v_cvt_pk_f16_f32 v212, v218, v219
	v_cvt_pk_f16_f32 v213, v220, v221
	ds_write_b128 v173, v[190:193]
	ds_write_b128 v172, v[194:197]
	ds_write_b128 v173, v[206:209] offset:32768
	ds_write_b128 v172, v[210:213] offset:32768
	v_xor_b32_e32 v255, 24, v254
	ds_read2_b64 v[238:241], v255 offset0:0 offset1:16
	ds_read2_b64 v[242:245], v255 offset0:32 offset1:48
	v_mfma_f32_32x32x16_f16 v[2:17], v[222:225], v[246:249], 0
	v_mfma_f32_32x32x16_f16 v[18:33], v[226:229], v[250:253], 0
	v_cvt_pk_f16_f32 v34, v34, v35
	v_cvt_pk_f16_f32 v35, v36, v37
	v_cvt_pk_f16_f32 v36, v38, v39
	v_cvt_pk_f16_f32 v37, v40, v41
	v_cvt_pk_f16_f32 v38, v42, v43
	v_cvt_pk_f16_f32 v39, v44, v45
	v_cvt_pk_f16_f32 v40, v46, v47
	v_cvt_pk_f16_f32 v41, v48, v49
	v_cvt_pk_f16_f32 v50, v50, v51
	v_cvt_pk_f16_f32 v51, v52, v53
	v_cvt_pk_f16_f32 v52, v54, v55
	v_cvt_pk_f16_f32 v53, v56, v57
	v_cvt_pk_f16_f32 v54, v58, v59
	v_cvt_pk_f16_f32 v55, v60, v61
	v_cvt_pk_f16_f32 v56, v62, v63
	v_cvt_pk_f16_f32 v57, v64, v65
	v_mfma_f32_32x32x16_f16 v[190:205], v[34:37], v[118:121], 0
	v_cvt_pk_f16_f32 v2, v2, v3
	v_cvt_pk_f16_f32 v3, v4, v5
	v_cvt_pk_f16_f32 v4, v6, v7
	v_cvt_pk_f16_f32 v5, v8, v9
	v_mfma_f32_32x32x16_f16 v[206:221], v[34:37], v[102:105], 0
	v_cvt_pk_f16_f32 v6, v10, v11
	v_cvt_pk_f16_f32 v7, v12, v13
	v_cvt_pk_f16_f32 v8, v14, v15
	v_cvt_pk_f16_f32 v9, v16, v17
	v_cvt_pk_f16_f32 v18, v18, v19
	v_mfma_f32_32x32x16_f16 v[190:205], v[38:41], v[114:117], v[190:205]
	v_cvt_pk_f16_f32 v19, v20, v21
	v_cvt_pk_f16_f32 v20, v22, v23
	v_cvt_pk_f16_f32 v21, v24, v25
	v_cvt_pk_f16_f32 v22, v26, v27
	v_mfma_f32_32x32x16_f16 v[206:221], v[38:41], v[98:101], v[206:221]
	v_cvt_pk_f16_f32 v23, v28, v29
	v_cvt_pk_f16_f32 v24, v30, v31
	v_cvt_pk_f16_f32 v25, v32, v33
	s_waitcnt lgkmcnt(0)
	v_mul_f32_e32 v66, v231, v239
	v_mfma_f32_32x32x16_f16 v[190:205], v[50:53], v[110:113], v[190:205]
	v_mul_f32_e32 v68, v231, v238
	v_mul_f32_e32 v67, v231, v241
	v_mul_f32_e32 v69, v231, v240
	v_fma_f32 v66, v230, v238, -v66
	v_fma_f32 v68, v230, v239, v68
	v_mfma_f32_32x32x16_f16 v[206:221], v[50:53], v[94:97], v[206:221]
	v_fma_f32 v67, v230, v240, -v67
	v_fma_f32 v69, v230, v241, v69
	v_cvt_pk_f16_f32 v246, v66, v67
	v_cvt_pk_f16_f32 v248, v68, v69
	v_mfma_f32_32x32x16_f16 v[190:205], v[54:57], v[106:109], v[190:205]
	v_mul_f32_e32 v70, v233, v243
	v_mul_f32_e32 v72, v233, v242
	v_mul_f32_e32 v71, v233, v245
	v_mul_f32_e32 v73, v233, v244
	v_fma_f32 v70, v232, v242, -v70
	v_mfma_f32_32x32x16_f16 v[206:221], v[54:57], v[90:93], v[206:221]
	v_fma_f32 v72, v232, v243, v72
	v_fma_f32 v71, v232, v244, -v71
	v_fma_f32 v73, v232, v245, v73
	v_cvt_pk_f16_f32 v247, v70, v71
	v_cvt_pk_f16_f32 v249, v72, v73
	v_mfma_f32_32x32x16_f16 v[34:49], v[2:5], v[150:153], 0
	v_mul_f32_e32 v66, v235, v239
	v_mul_f32_e32 v68, v235, v238
	v_mul_f32_e32 v67, v235, v241
	v_mul_f32_e32 v69, v235, v240
	v_fma_f32 v66, v234, v238, -v66
	v_mfma_f32_32x32x16_f16 v[34:49], v[18:21], v[146:149], v[34:49]
	v_fma_f32 v68, v234, v239, v68
	v_fma_f32 v67, v234, v240, -v67
	v_fma_f32 v69, v234, v241, v69
	v_cvt_pk_f16_f32 v250, v66, v67
	v_cvt_pk_f16_f32 v252, v68, v69
	v_mfma_f32_32x32x16_f16 v[34:49], v[6:9], v[142:145], v[34:49]
	v_mul_f32_e32 v70, v237, v243
	v_mul_f32_e32 v72, v237, v242
	v_mul_f32_e32 v71, v237, v245
	v_mul_f32_e32 v73, v237, v244
	v_fma_f32 v70, v236, v242, -v70
	v_mfma_f32_32x32x16_f16 v[34:49], v[22:25], v[138:141], v[34:49]
	v_fma_f32 v72, v236, v243, v72
	v_fma_f32 v71, v236, v244, -v71
	v_fma_f32 v73, v236, v245, v73
	v_cvt_pk_f16_f32 v251, v70, v71
	v_cvt_pk_f16_f32 v253, v72, v73
	v_cvt_pk_f16_f32 v190, v190, v191
	v_mfma_f32_32x32x16_f16 v[50:65], v[2:5], v[134:137], 0
	v_cvt_pk_f16_f32 v191, v192, v193
	v_cvt_pk_f16_f32 v192, v194, v195
	v_cvt_pk_f16_f32 v193, v196, v197
	v_cvt_pk_f16_f32 v194, v198, v199
	v_cvt_pk_f16_f32 v195, v200, v201
	v_mfma_f32_32x32x16_f16 v[50:65], v[18:21], v[126:129], v[50:65]
	v_cvt_pk_f16_f32 v196, v202, v203
	v_cvt_pk_f16_f32 v197, v204, v205
	v_cvt_pk_f16_f32 v206, v206, v207
	v_cvt_pk_f16_f32 v207, v208, v209
	v_cvt_pk_f16_f32 v208, v210, v211
	v_mfma_f32_32x32x16_f16 v[50:65], v[6:9], v[122:125], v[50:65]
	v_cvt_pk_f16_f32 v209, v212, v213
	v_cvt_pk_f16_f32 v210, v214, v215
	v_cvt_pk_f16_f32 v211, v216, v217
	v_cvt_pk_f16_f32 v212, v218, v219
	v_cvt_pk_f16_f32 v213, v220, v221
	v_mfma_f32_32x32x16_f16 v[50:65], v[22:25], v[130:133], v[50:65]
	v_xor_b32_e32 v74, 0x8a0, v173
	v_xor_b32_e32 v75, 0x8a0, v172
	ds_write_b128 v74, v[190:193]
	ds_write_b128 v75, v[194:197]
	ds_write_b128 v74, v[206:209] offset:32768
	ds_write_b128 v75, v[210:213] offset:32768
	s_nop 0
	v_mfma_f32_32x32x16_f16 v[2:17], v[222:225], v[246:249], 0
	v_mfma_f32_32x32x16_f16 v[18:33], v[226:229], v[250:253], 0
	v_cvt_pk_f16_f32 v34, v34, v35
	v_cvt_pk_f16_f32 v35, v36, v37
	v_cvt_pk_f16_f32 v36, v38, v39
	v_cvt_pk_f16_f32 v37, v40, v41
	v_cvt_pk_f16_f32 v38, v42, v43
	v_cvt_pk_f16_f32 v39, v44, v45
	v_cvt_pk_f16_f32 v40, v46, v47
	v_cvt_pk_f16_f32 v41, v48, v49
	v_cvt_pk_f16_f32 v50, v50, v51
	v_cvt_pk_f16_f32 v51, v52, v53
	v_cvt_pk_f16_f32 v52, v54, v55
	v_cvt_pk_f16_f32 v53, v56, v57
	v_cvt_pk_f16_f32 v54, v58, v59
	v_cvt_pk_f16_f32 v55, v60, v61
	v_cvt_pk_f16_f32 v56, v62, v63
	v_cvt_pk_f16_f32 v57, v64, v65
	v_mfma_f32_32x32x16_f16 v[190:205], v[34:37], v[118:121], 0
	v_cvt_pk_f16_f32 v2, v2, v3
	v_cvt_pk_f16_f32 v3, v4, v5
	v_mfma_f32_32x32x16_f16 v[206:221], v[34:37], v[102:105], 0
	v_cvt_pk_f16_f32 v4, v6, v7
	v_cvt_pk_f16_f32 v5, v8, v9
	v_mfma_f32_32x32x16_f16 v[190:205], v[38:41], v[114:117], v[190:205]
	v_cvt_pk_f16_f32 v6, v10, v11
	v_cvt_pk_f16_f32 v7, v12, v13
	v_mfma_f32_32x32x16_f16 v[206:221], v[38:41], v[98:101], v[206:221]
	v_cvt_pk_f16_f32 v8, v14, v15
	v_cvt_pk_f16_f32 v9, v16, v17
	v_mfma_f32_32x32x16_f16 v[190:205], v[50:53], v[110:113], v[190:205]
	v_cvt_pk_f16_f32 v18, v18, v19
	v_cvt_pk_f16_f32 v19, v20, v21
	v_mfma_f32_32x32x16_f16 v[206:221], v[50:53], v[94:97], v[206:221]
	v_cvt_pk_f16_f32 v20, v22, v23
	v_cvt_pk_f16_f32 v21, v24, v25
	v_mfma_f32_32x32x16_f16 v[190:205], v[54:57], v[106:109], v[190:205]
	v_cvt_pk_f16_f32 v22, v26, v27
	v_cvt_pk_f16_f32 v23, v28, v29
	v_mfma_f32_32x32x16_f16 v[206:221], v[54:57], v[90:93], v[206:221]
	v_cvt_pk_f16_f32 v24, v30, v31
	v_cvt_pk_f16_f32 v25, v32, v33
	v_mfma_f32_32x32x16_f16 v[34:49], v[2:5], v[150:153], 0
	v_mfma_f32_32x32x16_f16 v[34:49], v[18:21], v[146:149], v[34:49]
	v_mfma_f32_32x32x16_f16 v[34:49], v[6:9], v[142:145], v[34:49]
	v_mfma_f32_32x32x16_f16 v[34:49], v[22:25], v[138:141], v[34:49]
	v_mfma_f32_32x32x16_f16 v[50:65], v[2:5], v[134:137], 0
	s_nop 5
	v_cvt_pk_f16_f32 v190, v190, v191
	v_cvt_pk_f16_f32 v191, v192, v193
	v_cvt_pk_f16_f32 v192, v194, v195
	v_cvt_pk_f16_f32 v193, v196, v197
	v_mfma_f32_32x32x16_f16 v[50:65], v[18:21], v[126:129], v[50:65]
	v_cvt_pk_f16_f32 v194, v198, v199
	v_cvt_pk_f16_f32 v195, v200, v201
	v_cvt_pk_f16_f32 v196, v202, v203
	v_cvt_pk_f16_f32 v197, v204, v205
	v_cvt_pk_f16_f32 v206, v206, v207
	v_cvt_pk_f16_f32 v207, v208, v209
	v_mfma_f32_32x32x16_f16 v[50:65], v[6:9], v[122:125], v[50:65]
	v_cvt_pk_f16_f32 v208, v210, v211
	v_cvt_pk_f16_f32 v209, v212, v213
	v_cvt_pk_f16_f32 v210, v214, v215
	v_cvt_pk_f16_f32 v211, v216, v217
	v_cvt_pk_f16_f32 v212, v218, v219
	v_cvt_pk_f16_f32 v213, v220, v221
	v_mfma_f32_32x32x16_f16 v[50:65], v[22:25], v[130:133], v[50:65]
	v_xor_b32_e32 v74, 0x1040, v173
	v_xor_b32_e32 v75, 0x1040, v172
	ds_write_b128 v74, v[190:193]
	ds_write_b128 v75, v[194:197]
	ds_write_b128 v74, v[206:209] offset:32768
	ds_write_b128 v75, v[210:213] offset:32768
	s_nop 11
	v_cvt_pk_f16_f32 v34, v34, v35
	v_cvt_pk_f16_f32 v35, v36, v37
	v_cvt_pk_f16_f32 v36, v38, v39
	v_cvt_pk_f16_f32 v37, v40, v41
	v_cvt_pk_f16_f32 v38, v42, v43
	v_cvt_pk_f16_f32 v39, v44, v45
	v_cvt_pk_f16_f32 v40, v46, v47
	v_cvt_pk_f16_f32 v41, v48, v49
	v_cvt_pk_f16_f32 v50, v50, v51
	v_cvt_pk_f16_f32 v51, v52, v53
	v_cvt_pk_f16_f32 v52, v54, v55
	v_cvt_pk_f16_f32 v53, v56, v57
	v_cvt_pk_f16_f32 v54, v58, v59
	v_cvt_pk_f16_f32 v55, v60, v61
	v_cvt_pk_f16_f32 v56, v62, v63
	v_cvt_pk_f16_f32 v57, v64, v65
	v_mfma_f32_32x32x16_f16 v[190:205], v[34:37], v[118:121], 0
	v_mfma_f32_32x32x16_f16 v[206:221], v[34:37], v[102:105], 0
	v_mfma_f32_32x32x16_f16 v[190:205], v[38:41], v[114:117], v[190:205]
	v_mfma_f32_32x32x16_f16 v[206:221], v[38:41], v[98:101], v[206:221]
	v_mfma_f32_32x32x16_f16 v[190:205], v[50:53], v[110:113], v[190:205]
	v_mfma_f32_32x32x16_f16 v[206:221], v[50:53], v[94:97], v[206:221]
	v_mfma_f32_32x32x16_f16 v[190:205], v[54:57], v[106:109], v[190:205]
	v_mfma_f32_32x32x16_f16 v[206:221], v[54:57], v[90:93], v[206:221]
	v_and_b32_e32 v134, 1, v156
	v_bitop3_b32 v132, v171, s40, v170 bitop3:0x36
	v_bitop3_b32 v131, s41, v154, v160 bitop3:0x36
	v_bitop3_b32 v135, v171, s42, v170 bitop3:0x36
	v_xor_b32_e32 v133, s43, v154
	v_and_b32_e32 v130, 4, v156
	s_lshl_b32 s2, s27, 3
	s_lshl_b32 s3, s5, 2
	s_or_b32 s2, s3, s2
	s_ashr_i32 s3, s2, 31
	s_lshl_b64 s[2:3], s[2:3], 13
	s_add_u32 s2, s20, s2
	s_addc_u32 s3, s21, s3
	v_lshlrev_b32_e32 v154, 1, v169
	v_lshl_add_u64 v[2:3], s[2:3], 0, v[154:155]
	v_add_co_u32_e32 v2, vcc, s23, v2
	s_nop 1
	v_addc_co_u32_e32 v3, vcc, 0, v3, vcc
	v_cvt_pk_f16_f32 v190, v190, v191
	v_cvt_pk_f16_f32 v191, v192, v193
	v_cvt_pk_f16_f32 v192, v194, v195
	v_cvt_pk_f16_f32 v193, v196, v197
	v_cvt_pk_f16_f32 v194, v198, v199
	v_cvt_pk_f16_f32 v195, v200, v201
	v_cvt_pk_f16_f32 v196, v202, v203
	v_cvt_pk_f16_f32 v197, v204, v205
	v_cvt_pk_f16_f32 v206, v206, v207
	v_cvt_pk_f16_f32 v207, v208, v209
	v_cvt_pk_f16_f32 v208, v210, v211
	v_cvt_pk_f16_f32 v209, v212, v213
	v_cvt_pk_f16_f32 v210, v214, v215
	v_cvt_pk_f16_f32 v211, v216, v217
	v_cvt_pk_f16_f32 v212, v218, v219
	v_cvt_pk_f16_f32 v213, v220, v221
	v_xor_b32_e32 v74, 0x18e0, v173
	v_xor_b32_e32 v75, 0x18e0, v172
	ds_write_b128 v74, v[190:193]
	ds_write_b128 v75, v[194:197]
	ds_write_b128 v74, v[206:209] offset:32768
	ds_write_b128 v75, v[210:213] offset:32768
	s_setprio 0
	s_waitcnt lgkmcnt(0)
	s_barrier
	global_load_dwordx4 v[62:65], v154, s[2:3]
	global_load_dwordx4 v[46:49], v154, s[2:3] offset:1024
	global_load_dwordx4 v[42:45], v154, s[2:3] offset:2048
	global_load_dwordx4 v[38:41], v154, s[2:3] offset:3072
	global_load_dwordx4 v[54:57], v[2:3], off offset:1024
	global_load_dwordx4 v[50:53], v[2:3], off offset:2048
	v_lshl_add_u64 v[4:5], s[12:13], 0, v[154:155]
	global_load_dwordx4 v[126:129], v154, s[12:13]
	global_load_dwordx4 v[122:125], v154, s[12:13] offset:1024
	global_load_dwordx4 v[118:121], v154, s[12:13] offset:2048
	global_load_dwordx4 v[114:117], v154, s[12:13] offset:3072
	global_load_dwordx4 v[34:37], v168, s[2:3]
	global_load_dwordx4 v[110:113], v168, s[12:13]
	v_add_co_u32_e32 v4, vcc, s23, v4
	s_nop 1
	v_addc_co_u32_e32 v5, vcc, 0, v5, vcc
	global_load_dwordx4 v[58:61], v[2:3], off offset:3072
	global_load_dwordx4 v[106:109], v[4:5], off offset:1024
	global_load_dwordx4 v[94:97], v[4:5], off offset:2048
	global_load_dwordx4 v[90:93], v[4:5], off offset:3072
	v_bfrev_b32_e32 v3, v156
	v_lshlrev_b32_e32 v7, 5, v167
	v_lshlrev_b32_e32 v6, 9, v167
	v_and_b32_e32 v7, 0x200, v7
	v_lshlrev_b32_e32 v8, 8, v167
	v_lshrrev_b32_e32 v3, 27, v3
	v_lshrrev_b32_e32 v2, 2, v167
	v_lshrrev_b32_e32 v4, 4, v156
	v_xor_b32_e32 v5, v169, v156
	v_and_b32_e32 v6, 0x5800, v6
	v_and_b32_e32 v3, 8, v3
	v_and_or_b32 v7, v8, s24, v7
	v_lshrrev_b32_e32 v5, 1, v5
	v_xor_b32_e32 v4, v2, v4
	v_or3_b32 v3, v7, v6, v3
	v_bitop3_b32 v7, v2, v182, 1 bitop3:0x6c
	v_lshlrev_b32_e32 v2, 1, v167
	v_and_b32_e32 v5, 4, v5
	v_lshlrev_b32_e32 v4, 3, v4
	v_lshrrev_b32_e32 v6, 1, v167
	v_and_b32_e32 v2, 2, v2
	v_and_or_b32 v9, v169, 8, v2
	v_and_b32_e32 v2, 8, v4
	v_and_or_b32 v4, v6, 2, v5
	v_or3_b32 v2, v4, v2, v134
	v_lshlrev_b32_e32 v2, 4, v2
	v_bitop3_b32 v146, v3, s28, v2 bitop3:0x36
	v_xor_b32_e32 v8, v6, v182
	v_xor_b32_e32 v147, 0x2010, v146
	v_lshlrev_b32_e32 v8, 2, v8
	v_and_b32_e32 v8, 4, v8
	v_or3_b32 v6, v9, v7, v8
	v_lshlrev_b32_e32 v7, 11, v167
	v_and_b32_e32 v8, 0x7800, v7
	v_lshlrev_b32_e32 v6, 4, v6
	v_or3_b32 v22, v6, v8, v170
	v_and_b32_e32 v23, 0x8000, v7
	v_xor_b32_e32 v150, 16, v146
	v_xad_u32 v70, v22, s28, v23
	v_xor_b32_e32 v151, 0x2000, v146
	ds_read_b64_tr_b16 v[18:19], v146
	ds_read_b64_tr_b16 v[20:21], v147
	ds_read_b64_tr_b16 v[22:23], v146 offset:32768
	ds_read_b64_tr_b16 v[24:25], v147 offset:32768
	ds_read_b64_tr_b16 v[26:27], v150
	ds_read_b64_tr_b16 v[28:29], v151
	ds_read_b64_tr_b16 v[30:31], v150 offset:32768
	ds_read_b64_tr_b16 v[32:33], v151 offset:32768
	v_xor_b32_e32 v148, 32, v146
	v_xor_b32_e32 v149, 0x2030, v146
	v_xor_b32_e32 v144, 48, v146
	v_xor_b32_e32 v145, 0x2020, v146
	v_xor_b32_e32 v142, 64, v146
	v_xor_b32_e32 v143, 0x2050, v146
	v_xor_b32_e32 v140, 0x50, v146
	v_xor_b32_e32 v141, 0x2040, v146
	v_xor_b32_e32 v138, 0x60, v146
	v_xor_b32_e32 v139, 0x2070, v146
	v_xor_b32_e32 v136, 0x70, v146
	v_xor_b32_e32 v137, 0x2060, v146
	v_xor_b32_e32 v71, 0x60, v70
	s_lshl_b64 s[0:1], s[0:1], 13
	s_add_u32 s0, s8, s0
	s_addc_u32 s1, s9, s1
	s_waitcnt vmcnt(17) lgkmcnt(4)
	v_mfma_f32_32x32x16_f16 v[2:17], v[18:21], v[86:89], 0
	s_waitcnt vmcnt(16)
	v_mfma_f32_32x32x16_f16 v[2:17], v[22:25], v[82:85], v[2:17]
	ds_read_b64_tr_b16 v[206:207], v148
	ds_read_b64_tr_b16 v[208:209], v149
	ds_read_b64_tr_b16 v[210:211], v148 offset:32768
	ds_read_b64_tr_b16 v[212:213], v149 offset:32768
	s_waitcnt lgkmcnt(4)
	v_mfma_f32_32x32x16_f16 v[190:205], v[26:29], v[86:89], 0
	v_mfma_f32_32x32x16_f16 v[190:205], v[30:33], v[82:85], v[190:205]
	s_nop 4
	v_cvt_pk_f16_f32 v2, v2, v3
	v_cvt_pk_f16_f32 v3, v4, v5
	v_cvt_pk_f16_f32 v4, v6, v7
	v_cvt_pk_f16_f32 v5, v8, v9
	v_cvt_pk_f16_f32 v6, v10, v11
	v_cvt_pk_f16_f32 v7, v12, v13
	v_cvt_pk_f16_f32 v8, v14, v15
	v_cvt_pk_f16_f32 v9, v16, v17
	v_xor_b32_e32 v73, 0x280, v70
	ds_write_b128 v70, v[2:5]
	ds_write_b128 v73, v[6:9]
	ds_read_b64_tr_b16 v[18:19], v144
	ds_read_b64_tr_b16 v[20:21], v145
	ds_read_b64_tr_b16 v[22:23], v144 offset:32768
	ds_read_b64_tr_b16 v[24:25], v145 offset:32768
	s_waitcnt lgkmcnt(6)
	v_mfma_f32_32x32x16_f16 v[2:17], v[206:209], v[86:89], 0
	v_mfma_f32_32x32x16_f16 v[2:17], v[210:213], v[82:85], v[2:17]
	v_cvt_pk_f16_f32 v190, v190, v191
	v_cvt_pk_f16_f32 v191, v192, v193
	v_cvt_pk_f16_f32 v192, v194, v195
	v_cvt_pk_f16_f32 v193, v196, v197
	v_cvt_pk_f16_f32 v194, v198, v199
	v_cvt_pk_f16_f32 v195, v200, v201
	v_cvt_pk_f16_f32 v196, v202, v203
	v_cvt_pk_f16_f32 v197, v204, v205
	v_xor_b32_e32 v72, 16, v70
	v_xor_b32_e32 v73, 0x290, v70
	ds_write_b128 v72, v[190:193]
	ds_write_b128 v73, v[194:197]
	ds_read_b64_tr_b16 v[26:27], v142
	ds_read_b64_tr_b16 v[28:29], v143
	ds_read_b64_tr_b16 v[30:31], v142 offset:32768
	ds_read_b64_tr_b16 v[32:33], v143 offset:32768
	s_waitcnt lgkmcnt(6)
	v_mfma_f32_32x32x16_f16 v[190:205], v[18:21], v[86:89], 0
	v_mfma_f32_32x32x16_f16 v[190:205], v[22:25], v[82:85], v[190:205]
	v_cvt_pk_f16_f32 v2, v2, v3
	v_cvt_pk_f16_f32 v3, v4, v5
	v_cvt_pk_f16_f32 v4, v6, v7
	v_cvt_pk_f16_f32 v5, v8, v9
	v_cvt_pk_f16_f32 v6, v10, v11
	v_cvt_pk_f16_f32 v7, v12, v13
	v_cvt_pk_f16_f32 v8, v14, v15
	v_cvt_pk_f16_f32 v9, v16, v17
	v_xor_b32_e32 v72, 32, v70
	v_xor_b32_e32 v73, 0x2a0, v70
	ds_write_b128 v72, v[2:5]
	ds_write_b128 v73, v[6:9]
	ds_read_b64_tr_b16 v[206:207], v140
	ds_read_b64_tr_b16 v[208:209], v141
	ds_read_b64_tr_b16 v[210:211], v140 offset:32768
	ds_read_b64_tr_b16 v[212:213], v141 offset:32768
	s_waitcnt lgkmcnt(6)
	v_mfma_f32_32x32x16_f16 v[2:17], v[26:29], v[86:89], 0
	v_mfma_f32_32x32x16_f16 v[2:17], v[30:33], v[82:85], v[2:17]
	v_cvt_pk_f16_f32 v190, v190, v191
	v_cvt_pk_f16_f32 v191, v192, v193
	v_cvt_pk_f16_f32 v192, v194, v195
	v_cvt_pk_f16_f32 v193, v196, v197
	v_cvt_pk_f16_f32 v194, v198, v199
	v_cvt_pk_f16_f32 v195, v200, v201
	v_cvt_pk_f16_f32 v196, v202, v203
	v_cvt_pk_f16_f32 v197, v204, v205
	v_xor_b32_e32 v72, 48, v70
	v_xor_b32_e32 v73, 0x2b0, v70
	ds_write_b128 v72, v[190:193]
	ds_write_b128 v73, v[194:197]
	ds_read_b64_tr_b16 v[18:19], v138
	ds_read_b64_tr_b16 v[20:21], v139
	ds_read_b64_tr_b16 v[22:23], v138 offset:32768
	ds_read_b64_tr_b16 v[24:25], v139 offset:32768
	s_waitcnt lgkmcnt(6)
	v_mfma_f32_32x32x16_f16 v[190:205], v[206:209], v[86:89], 0
	v_mfma_f32_32x32x16_f16 v[190:205], v[210:213], v[82:85], v[190:205]
	v_cvt_pk_f16_f32 v2, v2, v3
	v_cvt_pk_f16_f32 v3, v4, v5
	v_cvt_pk_f16_f32 v4, v6, v7
	v_cvt_pk_f16_f32 v5, v8, v9
	v_cvt_pk_f16_f32 v6, v10, v11
	v_cvt_pk_f16_f32 v7, v12, v13
	v_cvt_pk_f16_f32 v8, v14, v15
	v_cvt_pk_f16_f32 v9, v16, v17
	v_xor_b32_e32 v72, 64, v70
	v_xor_b32_e32 v73, 0x2c0, v70
	ds_write_b128 v72, v[2:5]
	ds_write_b128 v73, v[6:9]
	ds_read_b64_tr_b16 v[26:27], v136
	ds_read_b64_tr_b16 v[28:29], v137
	ds_read_b64_tr_b16 v[30:31], v136 offset:32768
	ds_read_b64_tr_b16 v[32:33], v137 offset:32768
	s_waitcnt lgkmcnt(6)
	v_mfma_f32_32x32x16_f16 v[2:17], v[18:21], v[86:89], 0
	v_mfma_f32_32x32x16_f16 v[2:17], v[22:25], v[82:85], v[2:17]
	v_cvt_pk_f16_f32 v190, v190, v191
	v_cvt_pk_f16_f32 v191, v192, v193
	v_cvt_pk_f16_f32 v192, v194, v195
	v_cvt_pk_f16_f32 v193, v196, v197
	v_cvt_pk_f16_f32 v194, v198, v199
	v_cvt_pk_f16_f32 v195, v200, v201
	v_cvt_pk_f16_f32 v196, v202, v203
	v_cvt_pk_f16_f32 v197, v204, v205
	v_xor_b32_e32 v72, 0x50, v70
	v_xor_b32_e32 v73, 0x2d0, v70
	ds_write_b128 v72, v[190:193]
	ds_write_b128 v73, v[194:197]
	s_waitcnt lgkmcnt(2)
	v_mfma_f32_32x32x16_f16 v[190:205], v[26:29], v[86:89], 0
	v_mfma_f32_32x32x16_f16 v[190:205], v[30:33], v[82:85], v[190:205]
	v_cvt_pk_f16_f32 v2, v2, v3
	v_cvt_pk_f16_f32 v3, v4, v5
	v_cvt_pk_f16_f32 v4, v6, v7
	v_cvt_pk_f16_f32 v5, v8, v9
	v_cvt_pk_f16_f32 v6, v10, v11
	v_cvt_pk_f16_f32 v7, v12, v13
	v_cvt_pk_f16_f32 v8, v14, v15
	v_cvt_pk_f16_f32 v9, v16, v17
	v_xor_b32_e32 v72, 0x60, v70
	v_xor_b32_e32 v73, 0x2e0, v70
	ds_write_b128 v72, v[2:5]
	ds_write_b128 v73, v[6:9]
	v_cvt_pk_f16_f32 v190, v190, v191
	v_cvt_pk_f16_f32 v191, v192, v193
	v_cvt_pk_f16_f32 v192, v194, v195
	v_cvt_pk_f16_f32 v193, v196, v197
	v_cvt_pk_f16_f32 v194, v198, v199
	v_cvt_pk_f16_f32 v195, v200, v201
	v_cvt_pk_f16_f32 v196, v202, v203
	v_cvt_pk_f16_f32 v197, v204, v205
	v_xor_b32_e32 v72, 0x70, v70
	v_xor_b32_e32 v73, 0x2f0, v70
	ds_write_b128 v72, v[190:193]
	ds_write_b128 v73, v[194:197]
	v_lshl_add_u64 v[2:3], s[0:1], 0, v[154:155]
	v_lshl_add_u64 v[4:5], v[2:3], 0, s[18:19]
	v_add_co_u32_e32 v2, vcc, s25, v2
	s_waitcnt lgkmcnt(0)
	s_nop 0
	v_addc_co_u32_e32 v3, vcc, 0, v3, vcc
	s_barrier
	s_nop 0
	s_nop 0
	global_load_dwordx4 v[102:105], v[2:3], off
	global_load_dwordx4 v[98:101], v[4:5], off offset:1024
	s_setprio 1
	s_add_u32 s0, s2, 0x2000
	s_addc_u32 s1, s3, 0
	v_lshl_add_u64 v[2:3], s[0:1], 0, v[154:155]
	v_add_co_u32_e32 v2, vcc, s23, v2
	global_load_dwordx4 v[66:69], v154, s[0:1]
	global_load_dwordx4 v[70:73], v154, s[0:1] offset:1024
	global_load_dwordx4 v[74:77], v154, s[0:1] offset:2048
	global_load_dwordx4 v[78:81], v154, s[0:1] offset:3072
	v_addc_co_u32_e32 v3, vcc, 0, v3, vcc
	global_load_dwordx4 v[82:85], v168, s[0:1]
	global_load_dwordx4 v[86:89], v[2:3], off offset:1024
	global_load_dwordx4 v[182:185], v[2:3], off offset:2048
	global_load_dwordx4 v[186:189], v[2:3], off offset:3072
	ds_read_b128 v[18:21], v179
	ds_read_b128 v[22:25], v179 offset:32768
	ds_read_b128 v[26:29], v178
	ds_read_b128 v[30:33], v178 offset:32768
	s_add_u32 s0, s2, 0x6000
	s_addc_u32 s1, s3, 0
	s_waitcnt vmcnt(25) lgkmcnt(3)
	v_mfma_f32_32x32x16_f16 v[2:17], v[18:21], v[62:65], 0
	s_add_u32 s2, s2, 0x4000
	s_addc_u32 s3, s3, 0
	s_or_b32 s27, s26, 0x8a0
	s_or_b32 s26, s26, 0xa20
	s_waitcnt vmcnt(24) lgkmcnt(1)
	v_mfma_f32_32x32x16_f16 v[2:17], v[26:29], v[46:49], v[2:17]
	s_waitcnt vmcnt(23)
	v_mfma_f32_32x32x16_f16 v[2:17], v[22:25], v[42:45], v[2:17]
	s_waitcnt vmcnt(22) lgkmcnt(0)
	v_mfma_f32_32x32x16_f16 v[2:17], v[30:33], v[38:41], v[2:17]
	s_waitcnt vmcnt(15)
	v_mfma_f32_32x32x16_f16 v[34:49], v[18:21], v[34:37], 0
	s_nop 9
	v_cvt_pk_f16_f32 v9, v8, v9
	v_cvt_pk_f16_f32 v8, v6, v7
	v_cvt_pk_f16_f32 v7, v4, v5
	v_cvt_pk_f16_f32 v6, v2, v3
	v_cvt_pk_f16_f32 v5, v16, v17
	v_cvt_pk_f16_f32 v4, v14, v15
	v_cvt_pk_f16_f32 v3, v12, v13
	v_mfma_f32_32x32x16_f16 v[34:49], v[26:29], v[54:57], v[34:49]
	v_cvt_pk_f16_f32 v2, v10, v11
	v_mfma_f32_32x32x16_f16 v[34:49], v[22:25], v[50:53], v[34:49]
	s_waitcnt vmcnt(13)
	v_mfma_f32_32x32x16_f16 v[34:49], v[30:33], v[58:61], v[34:49]
	v_mfma_f32_32x32x16_f16 v[18:33], v[6:9], v[126:129], 0
	s_nop 10
	v_cvt_pk_f16_f32 v13, v40, v41
	v_cvt_pk_f16_f32 v12, v38, v39
	v_cvt_pk_f16_f32 v11, v36, v37
	v_cvt_pk_f16_f32 v10, v34, v35
	v_cvt_pk_f16_f32 v17, v48, v49
	v_cvt_pk_f16_f32 v16, v46, v47
	v_cvt_pk_f16_f32 v15, v44, v45
	v_mfma_f32_32x32x16_f16 v[50:65], v[6:9], v[110:113], 0
	v_bitop3_b32 v6, v171, s27, v170 bitop3:0x36
	v_cvt_pk_f16_f32 v14, v42, v43
	v_mfma_f32_32x32x16_f16 v[18:33], v[2:5], v[122:125], v[18:33]
	s_waitcnt vmcnt(12)
	v_mfma_f32_32x32x16_f16 v[50:65], v[2:5], v[106:109], v[50:65]
	ds_read_b128 v[2:5], v6
	ds_read_b128 v[6:9], v6 offset:32768
	v_mfma_f32_32x32x16_f16 v[18:33], v[10:13], v[118:121], v[18:33]
	s_waitcnt vmcnt(11)
	v_mfma_f32_32x32x16_f16 v[50:65], v[10:13], v[94:97], v[50:65]
	s_waitcnt vmcnt(7) lgkmcnt(1)
	v_mfma_f32_32x32x16_f16 v[34:49], v[2:5], v[66:69], 0
	v_mfma_f32_32x32x16_f16 v[18:33], v[14:17], v[114:117], v[18:33]
	v_mfma_f32_32x32x16_f16 v[50:65], v[14:17], v[90:93], v[50:65]
	v_bitop3_b32 v14, v171, s26, v170 bitop3:0x36
	ds_read_b128 v[10:13], v14
	ds_read_b128 v[14:17], v14 offset:32768
	s_nop 7
	v_cvt_pk_f16_f32 v25, v24, v25
	v_cvt_pk_f16_f32 v24, v22, v23
	v_cvt_pk_f16_f32 v23, v20, v21
	v_cvt_pk_f16_f32 v22, v18, v19
	v_cvt_pk_f16_f32 v21, v32, v33
	s_waitcnt vmcnt(6) lgkmcnt(1)
	v_mfma_f32_32x32x16_f16 v[34:49], v[10:13], v[70:73], v[34:49]
	v_cvt_pk_f16_f32 v20, v30, v31
	v_cvt_pk_f16_f32 v19, v28, v29
	v_cvt_pk_f16_f32 v18, v26, v27
	ds_write_b128 v173, v[22:25]
	ds_write_b128 v172, v[18:21]
	v_cvt_pk_f16_f32 v21, v56, v57
	v_cvt_pk_f16_f32 v20, v54, v55
	s_waitcnt vmcnt(5)
	v_mfma_f32_32x32x16_f16 v[34:49], v[6:9], v[74:77], v[34:49]
	v_cvt_pk_f16_f32 v19, v52, v53
	v_cvt_pk_f16_f32 v18, v50, v51
	ds_write_b128 v173, v[18:21] offset:32768
	v_cvt_pk_f16_f32 v21, v64, v65
	v_cvt_pk_f16_f32 v20, v62, v63
	v_cvt_pk_f16_f32 v19, v60, v61
	v_cvt_pk_f16_f32 v18, v58, v59
	s_waitcnt vmcnt(4) lgkmcnt(3)
	v_mfma_f32_32x32x16_f16 v[34:49], v[14:17], v[78:81], v[34:49]
	ds_write_b128 v172, v[18:21] offset:32768
	s_waitcnt vmcnt(3)
	v_mfma_f32_32x32x16_f16 v[66:81], v[2:5], v[82:85], 0
	s_nop 8
	v_cvt_pk_f16_f32 v41, v40, v41
	v_cvt_pk_f16_f32 v40, v38, v39
	v_cvt_pk_f16_f32 v39, v36, v37
	v_cvt_pk_f16_f32 v38, v34, v35
	v_cvt_pk_f16_f32 v85, v48, v49
	v_cvt_pk_f16_f32 v84, v46, v47
	v_cvt_pk_f16_f32 v83, v44, v45
	s_waitcnt vmcnt(2)
	v_mfma_f32_32x32x16_f16 v[66:81], v[10:13], v[86:89], v[66:81]
	v_cvt_pk_f16_f32 v82, v42, v43
	s_waitcnt vmcnt(1)
	v_mfma_f32_32x32x16_f16 v[66:81], v[6:9], v[182:185], v[66:81]
	s_waitcnt vmcnt(0)
	v_mfma_f32_32x32x16_f16 v[66:81], v[14:17], v[186:189], v[66:81]
	v_mfma_f32_32x32x16_f16 v[2:17], v[38:41], v[126:129], 0
	s_nop 10
	v_cvt_pk_f16_f32 v73, v72, v73
	v_cvt_pk_f16_f32 v72, v70, v71
	v_cvt_pk_f16_f32 v70, v66, v67
	v_cvt_pk_f16_f32 v67, v76, v77
	v_cvt_pk_f16_f32 v66, v74, v75
	global_load_dwordx4 v[74:77], v154, s[2:3]
	v_cvt_pk_f16_f32 v71, v68, v69
	v_cvt_pk_f16_f32 v69, v80, v81
	v_cvt_pk_f16_f32 v68, v78, v79
	global_load_dwordx4 v[78:81], v154, s[2:3] offset:1024
	ds_read_b128 v[18:21], v180
	ds_read_b128 v[22:25], v176
	ds_read_b128 v[26:29], v180 offset:32768
	global_load_dwordx4 v[30:33], v154, s[2:3] offset:2048
	v_mfma_f32_32x32x16_f16 v[34:49], v[38:41], v[110:113], 0
	v_mfma_f32_32x32x16_f16 v[2:17], v[82:85], v[122:125], v[2:17]
	v_mfma_f32_32x32x16_f16 v[34:49], v[82:85], v[106:109], v[34:49]
	ds_read_b128 v[82:85], v176 offset:32768
	s_waitcnt vmcnt(2) lgkmcnt(3)
	v_mfma_f32_32x32x16_f16 v[50:65], v[18:21], v[74:77], 0
	v_mfma_f32_32x32x16_f16 v[2:17], v[70:73], v[118:121], v[2:17]
	v_mfma_f32_32x32x16_f16 v[34:49], v[70:73], v[94:97], v[34:49]
	v_lshl_add_u64 v[70:71], s[2:3], 0, v[154:155]
	v_add_co_u32_e32 v152, vcc, s23, v70
	s_nop 1
	v_addc_co_u32_e32 v153, vcc, 0, v71, vcc
	s_waitcnt vmcnt(1) lgkmcnt(2)
	v_mfma_f32_32x32x16_f16 v[50:65], v[22:25], v[78:81], v[50:65]
	v_mfma_f32_32x32x16_f16 v[2:17], v[66:69], v[114:117], v[2:17]
	v_mfma_f32_32x32x16_f16 v[34:49], v[66:69], v[90:93], v[34:49]
	global_load_dwordx4 v[66:69], v154, s[2:3] offset:3072
	s_nop 9
	v_cvt_pk_f16_f32 v9, v8, v9
	v_cvt_pk_f16_f32 v8, v6, v7
	v_cvt_pk_f16_f32 v7, v4, v5
	v_cvt_pk_f16_f32 v6, v2, v3
	v_cvt_pk_f16_f32 v5, v16, v17
	v_cvt_pk_f16_f32 v4, v14, v15
	s_waitcnt vmcnt(1) lgkmcnt(1)
	v_mfma_f32_32x32x16_f16 v[50:65], v[26:29], v[30:33], v[50:65]
	global_load_dwordx4 v[30:33], v168, s[2:3]
	global_load_dwordx4 v[86:89], v[152:153], off offset:1024
	s_nop 0
	global_load_dwordx4 v[168:171], v168, s[0:1]
	v_cvt_pk_f16_f32 v3, v12, v13
	v_cvt_pk_f16_f32 v2, v10, v11
	ds_write_b128 v175, v[6:9]
	ds_write_b128 v174, v[2:5]
	v_cvt_pk_f16_f32 v5, v40, v41
	s_waitcnt vmcnt(3) lgkmcnt(2)
	v_mfma_f32_32x32x16_f16 v[50:65], v[82:85], v[66:69], v[50:65]
	global_load_dwordx4 v[182:185], v154, s[0:1] offset:1024
	v_cvt_pk_f16_f32 v4, v38, v39
	v_cvt_pk_f16_f32 v3, v36, v37
	v_cvt_pk_f16_f32 v2, v34, v35
	ds_write_b128 v175, v[2:5] offset:32768
	v_cvt_pk_f16_f32 v5, v48, v49
	v_cvt_pk_f16_f32 v4, v46, v47
	s_waitcnt vmcnt(3)
	v_mfma_f32_32x32x16_f16 v[66:81], v[18:21], v[30:33], 0
	global_load_dwordx4 v[18:21], v[152:153], off offset:2048
	v_cvt_pk_f16_f32 v3, v44, v45
	v_cvt_pk_f16_f32 v2, v42, v43
	ds_write_b128 v174, v[2:5] offset:32768
	v_cvt_pk_f16_f32 v57, v56, v57
	v_cvt_pk_f16_f32 v56, v54, v55
	v_cvt_pk_f16_f32 v55, v52, v53
	s_waitcnt vmcnt(3)
	v_mfma_f32_32x32x16_f16 v[66:81], v[22:25], v[86:89], v[66:81]
	global_load_dwordx4 v[22:25], v[152:153], off offset:3072
	v_cvt_pk_f16_f32 v54, v50, v51
	s_waitcnt vmcnt(1)
	v_mfma_f32_32x32x16_f16 v[66:81], v[26:29], v[18:21], v[66:81]
	v_lshl_add_u64 v[18:19], s[0:1], 0, v[154:155]
	v_add_co_u32_e32 v152, vcc, s23, v18
	s_nop 1
	v_addc_co_u32_e32 v153, vcc, 0, v19, vcc
	global_load_dwordx4 v[86:89], v[152:153], off offset:1024
	s_waitcnt vmcnt(1)
	v_mfma_f32_32x32x16_f16 v[66:81], v[82:85], v[22:25], v[66:81]
	v_cvt_pk_f16_f32 v85, v64, v65
	v_cvt_pk_f16_f32 v84, v62, v63
	v_cvt_pk_f16_f32 v83, v60, v61
	v_cvt_pk_f16_f32 v82, v58, v59
	v_mfma_f32_32x32x16_f16 v[18:33], v[54:57], v[126:129], 0
	s_nop 6
	v_cvt_pk_f16_f32 v73, v72, v73
	v_cvt_pk_f16_f32 v72, v70, v71
	v_cvt_pk_f16_f32 v70, v66, v67
	v_cvt_pk_f16_f32 v67, v76, v77
	v_cvt_pk_f16_f32 v66, v74, v75
	global_load_dwordx4 v[74:77], v154, s[0:1]
	ds_read_b128 v[2:5], v181
	ds_read_b128 v[6:9], v177
	ds_read_b128 v[10:13], v181 offset:32768
	global_load_dwordx4 v[14:17], v154, s[0:1] offset:2048
	global_load_dwordx4 v[34:37], v154, s[0:1] offset:3072
	v_mfma_f32_32x32x16_f16 v[50:65], v[54:57], v[110:113], 0
	v_cvt_pk_f16_f32 v71, v68, v69
	v_cvt_pk_f16_f32 v69, v80, v81
	v_cvt_pk_f16_f32 v68, v78, v79
	v_mfma_f32_32x32x16_f16 v[18:33], v[82:85], v[122:125], v[18:33]
	v_mfma_f32_32x32x16_f16 v[50:65], v[82:85], v[106:109], v[50:65]
	ds_read_b128 v[82:85], v177 offset:32768
	v_mfma_f32_32x32x16_f16 v[18:33], v[70:73], v[118:121], v[18:33]
	v_mfma_f32_32x32x16_f16 v[50:65], v[70:73], v[94:97], v[50:65]
	v_mfma_f32_32x32x16_f16 v[18:33], v[66:69], v[114:117], v[18:33]
	v_mfma_f32_32x32x16_f16 v[50:65], v[66:69], v[90:93], v[50:65]
	s_nop 10
	v_cvt_pk_f16_f32 v25, v24, v25
	v_cvt_pk_f16_f32 v24, v22, v23
	v_cvt_pk_f16_f32 v23, v20, v21
	v_cvt_pk_f16_f32 v22, v18, v19
	ds_write_b128 v132, v[22:25]
	s_waitcnt vmcnt(2) lgkmcnt(4)
	v_mfma_f32_32x32x16_f16 v[66:81], v[2:5], v[74:77], 0
	s_waitcnt lgkmcnt(3)
	v_mfma_f32_32x32x16_f16 v[66:81], v[6:9], v[182:185], v[66:81]
	s_waitcnt vmcnt(1) lgkmcnt(2)
	v_mfma_f32_32x32x16_f16 v[66:81], v[10:13], v[14:17], v[66:81]
	s_waitcnt vmcnt(0) lgkmcnt(1)
	v_mfma_f32_32x32x16_f16 v[66:81], v[82:85], v[34:37], v[66:81]
	v_mfma_f32_32x32x16_f16 v[34:49], v[2:5], v[168:171], 0
	global_load_dwordx4 v[2:5], v[152:153], off offset:2048
	s_nop 9
	v_cvt_pk_f16_f32 v73, v72, v73
	v_cvt_pk_f16_f32 v72, v70, v71
	v_cvt_pk_f16_f32 v71, v68, v69
	v_cvt_pk_f16_f32 v70, v66, v67
	v_cvt_pk_f16_f32 v69, v80, v81
	v_cvt_pk_f16_f32 v68, v78, v79
	v_mfma_f32_32x32x16_f16 v[34:49], v[6:9], v[86:89], v[34:49]
	global_load_dwordx4 v[6:9], v[152:153], off offset:3072
	v_cvt_pk_f16_f32 v67, v76, v77
	v_cvt_pk_f16_f32 v66, v74, v75
	s_waitcnt vmcnt(1)
	v_mfma_f32_32x32x16_f16 v[34:49], v[10:13], v[2:5], v[34:49]
	s_waitcnt vmcnt(0)
	v_mfma_f32_32x32x16_f16 v[34:49], v[82:85], v[6:9], v[34:49]
	v_mfma_f32_32x32x16_f16 v[2:17], v[70:73], v[126:129], 0
	s_nop 10
	v_cvt_pk_f16_f32 v41, v40, v41
	v_cvt_pk_f16_f32 v40, v38, v39
	v_cvt_pk_f16_f32 v38, v34, v35
	v_cvt_pk_f16_f32 v35, v44, v45
	v_cvt_pk_f16_f32 v34, v42, v43
	v_cvt_pk_f16_f32 v45, v32, v33
	v_cvt_pk_f16_f32 v44, v30, v31
	v_cvt_pk_f16_f32 v43, v28, v29
	v_cvt_pk_f16_f32 v42, v26, v27
	v_mfma_f32_32x32x16_f16 v[18:33], v[70:73], v[110:113], 0
	v_cvt_pk_f16_f32 v39, v36, v37
	v_cvt_pk_f16_f32 v37, v48, v49
	v_cvt_pk_f16_f32 v36, v46, v47
	ds_write_b128 v131, v[42:45]
	v_cvt_pk_f16_f32 v45, v56, v57
	v_cvt_pk_f16_f32 v44, v54, v55
	v_cvt_pk_f16_f32 v43, v52, v53
	v_mfma_f32_32x32x16_f16 v[2:17], v[66:69], v[122:125], v[2:17]
	v_cvt_pk_f16_f32 v42, v50, v51
	ds_write_b128 v132, v[42:45] offset:32768
	v_cvt_pk_f16_f32 v45, v64, v65
	v_cvt_pk_f16_f32 v44, v62, v63
	v_cvt_pk_f16_f32 v43, v60, v61
	v_cvt_pk_f16_f32 v42, v58, v59
	ds_write_b128 v131, v[42:45] offset:32768
	v_mfma_f32_32x32x16_f16 v[18:33], v[66:69], v[106:109], v[18:33]
	v_mfma_f32_32x32x16_f16 v[2:17], v[38:41], v[118:121], v[2:17]
	v_mfma_f32_32x32x16_f16 v[18:33], v[38:41], v[94:97], v[18:33]
	v_mfma_f32_32x32x16_f16 v[2:17], v[34:37], v[114:117], v[2:17]
	v_mfma_f32_32x32x16_f16 v[18:33], v[34:37], v[90:93], v[18:33]
	s_nop 10
	v_cvt_pk_f16_f32 v9, v8, v9
	v_cvt_pk_f16_f32 v8, v6, v7
	v_cvt_pk_f16_f32 v7, v4, v5
	v_cvt_pk_f16_f32 v6, v2, v3
	v_cvt_pk_f16_f32 v5, v16, v17
	v_cvt_pk_f16_f32 v4, v14, v15
	v_cvt_pk_f16_f32 v3, v12, v13
	v_cvt_pk_f16_f32 v2, v10, v11
	ds_write_b128 v135, v[6:9]
	ds_write_b128 v133, v[2:5]
	v_cvt_pk_f16_f32 v5, v24, v25
	v_cvt_pk_f16_f32 v4, v22, v23
	v_cvt_pk_f16_f32 v3, v20, v21
	v_cvt_pk_f16_f32 v2, v18, v19
	ds_write_b128 v135, v[2:5] offset:32768
	v_cvt_pk_f16_f32 v5, v32, v33
	v_cvt_pk_f16_f32 v4, v30, v31
	v_cvt_pk_f16_f32 v3, v28, v29
	v_cvt_pk_f16_f32 v2, v26, v27
	ds_write_b128 v133, v[2:5] offset:32768
	s_setprio 0
	s_waitcnt lgkmcnt(0)
	s_barrier
	ds_read_b64_tr_b16 v[2:3], v146
	ds_read_b64_tr_b16 v[4:5], v147
	ds_read_b64_tr_b16 v[36:37], v147 offset:32768
	ds_read_b64_tr_b16 v[34:35], v146 offset:32768
	ds_read_b64_tr_b16 v[18:19], v150
	ds_read_b64_tr_b16 v[20:21], v151
	ds_read_b64_tr_b16 v[40:41], v151 offset:32768
	ds_read_b64_tr_b16 v[38:39], v150 offset:32768
	s_waitcnt lgkmcnt(6)
	v_mfma_f32_32x32x16_f16 v[2:17], v[2:5], v[102:105], 0
	ds_read_b64_tr_b16 v[42:43], v148
	ds_read_b64_tr_b16 v[44:45], v149
	ds_read_b64_tr_b16 v[48:49], v149 offset:32768
	ds_read_b64_tr_b16 v[46:47], v148 offset:32768
	v_cmp_gt_u32_e64 s[0:1], 32, v167
	s_cmp_eq_u32 s5, 0
	v_cmp_lt_i32_e64 s[2:3], v162, v163
	s_waitcnt lgkmcnt(6)
	v_mfma_f32_32x32x16_f16 v[18:33], v[18:21], v[102:105], 0
	v_mfma_f32_32x32x16_f16 v[2:17], v[34:37], v[98:101], v[2:17]
	s_waitcnt lgkmcnt(4)
	v_mfma_f32_32x32x16_f16 v[18:33], v[38:41], v[98:101], v[18:33]
	s_nop 9
	v_mul_f32_e64 v34, v16, v16
	v_mul_f32_e64 v35, v17, v17
	v_mul_f32_e64 v36, v12, v12
	v_mul_f32_e64 v37, v13, v13
	v_mul_f32_e64 v50, v8, v8
	v_mul_f32_e64 v51, v9, v9
	v_pk_mul_f32 v[52:53], v[4:5], v[4:5]
	v_pk_fma_f32 v[50:51], v[6:7], v[6:7], v[50:51]
	v_pk_fma_f32 v[52:53], v[2:3], v[2:3], v[52:53]
	v_pk_fma_f32 v[36:37], v[10:11], v[10:11], v[36:37]
	v_pk_fma_f32 v[34:35], v[14:15], v[14:15], v[34:35]
	v_pk_mul_f32 v[116:117], v[24:25], v[24:25]
	v_pk_mul_f32 v[118:119], v[20:21], v[20:21]
	v_pk_add_f32 v[50:51], v[52:53], v[50:51]
	v_pk_add_f32 v[34:35], v[36:37], v[34:35]
	v_pk_mul_f32 v[112:113], v[32:33], v[32:33]
	v_pk_mul_f32 v[114:115], v[28:29], v[28:29]
	v_pk_mul_f32 v[120:121], v[18:19], v[18:19]
	v_pk_fma_f32 v[18:19], v[18:19], v[18:19], v[118:119]
	v_pk_fma_f32 v[20:21], v[22:23], v[22:23], v[116:117]
	v_pk_add_f32 v[34:35], v[50:51], v[34:35]
	v_pk_mul_f32 v[106:107], v[22:23], v[22:23]
	v_pk_add_f32 v[18:19], v[18:19], v[20:21]
	v_pk_fma_f32 v[20:21], v[26:27], v[26:27], v[114:115]
	v_pk_fma_f32 v[22:23], v[30:31], v[30:31], v[112:113]
	v_add_f32_e32 v34, v34, v35
	v_pk_add_f32 v[20:21], v[20:21], v[22:23]
	v_add_f32_e32 v36, 0, v34
	v_pk_mul_f32 v[108:109], v[26:27], v[26:27]
	v_pk_mul_f32 v[110:111], v[30:31], v[30:31]
	v_pk_add_f32 v[34:35], v[18:19], v[20:21]
	s_waitcnt lgkmcnt(2)
	v_mfma_f32_32x32x16_f16 v[18:33], v[42:45], v[102:105], 0
	v_add_f32_e32 v34, v34, v35
	v_add_f32_e32 v54, v36, v34
	v_sub_f32_e32 v55, v36, v34
	ds_read_b64_tr_b16 v[34:35], v144
	ds_read_b64_tr_b16 v[36:37], v145
	ds_read_b64_tr_b16 v[52:53], v145 offset:32768
	ds_read_b64_tr_b16 v[50:51], v144 offset:32768
	v_pk_fma_f32 v[4:5], v[4:5], v[4:5], v[118:119]
	v_pk_fma_f32 v[16:17], v[16:17], v[16:17], v[112:113]
	v_pk_fma_f32 v[14:15], v[14:15], v[14:15], v[110:111]
	s_waitcnt lgkmcnt(4)
	v_mfma_f32_32x32x16_f16 v[18:33], v[46:49], v[98:101], v[18:33]
	v_fma_f32 v12, v12, v12, v114
	v_fma_f32 v13, v13, v13, v115
	v_fma_f32 v10, v10, v10, v108
	v_fma_f32 v11, v11, v11, v109
	v_fma_f32 v8, v8, v8, v116
	v_fma_f32 v9, v9, v9, v117
	v_pk_fma_f32 v[6:7], v[6:7], v[6:7], v[106:107]
	v_pk_fma_f32 v[2:3], v[2:3], v[2:3], v[120:121]
	s_nop 3
	v_pk_mul_f32 v[38:39], v[32:33], v[32:33]
	v_pk_mul_f32 v[40:41], v[28:29], v[28:29]
	v_pk_mul_f32 v[42:43], v[24:25], v[24:25]
	v_pk_mul_f32 v[44:45], v[20:21], v[20:21]
	v_pk_fma_f32 v[42:43], v[22:23], v[22:23], v[42:43]
	v_pk_fma_f32 v[44:45], v[18:19], v[18:19], v[44:45]
	v_pk_fma_f32 v[40:41], v[26:27], v[26:27], v[40:41]
	v_pk_fma_f32 v[38:39], v[30:31], v[30:31], v[38:39]
	v_pk_add_f32 v[42:43], v[44:45], v[42:43]
	v_pk_add_f32 v[38:39], v[40:41], v[38:39]
	v_pk_fma_f32 v[4:5], v[20:21], v[20:21], v[4:5]
	v_pk_add_f32 v[38:39], v[42:43], v[38:39]
	v_pk_fma_f32 v[6:7], v[22:23], v[22:23], v[6:7]
	v_add_f32_e32 v56, v38, v39
	s_waitcnt lgkmcnt(2)
	v_mfma_f32_32x32x16_f16 v[34:49], v[34:37], v[102:105], 0
	v_add_f32_e32 v70, v54, v56
	v_add_f32_e32 v71, v55, v56
	v_sub_f32_e32 v72, v54, v56
	ds_read_b64_tr_b16 v[54:55], v142
	ds_read_b64_tr_b16 v[56:57], v143
	ds_read_b64_tr_b16 v[68:69], v143 offset:32768
	ds_read_b64_tr_b16 v[66:67], v142 offset:32768
	v_pk_fma_f32 v[8:9], v[24:25], v[24:25], v[8:9]
	v_pk_fma_f32 v[10:11], v[26:27], v[26:27], v[10:11]
	v_pk_fma_f32 v[12:13], v[28:29], v[28:29], v[12:13]
	s_waitcnt lgkmcnt(4)
	v_mfma_f32_32x32x16_f16 v[34:49], v[50:53], v[98:101], v[34:49]
	v_fma_f32 v14, v30, v30, v14
	v_fma_f32 v15, v31, v31, v15
	v_fma_f32 v16, v32, v32, v16
	v_fma_f32 v17, v33, v33, v17
	v_fma_f32 v2, v18, v18, v2
	v_fma_f32 v3, v19, v19, v3
	s_nop 5
	v_pk_mul_f32 v[50:51], v[48:49], v[48:49]
	v_pk_mul_f32 v[52:53], v[44:45], v[44:45]
	v_pk_mul_f32 v[58:59], v[40:41], v[40:41]
	v_pk_mul_f32 v[60:61], v[36:37], v[36:37]
	v_pk_fma_f32 v[58:59], v[38:39], v[38:39], v[58:59]
	v_pk_fma_f32 v[60:61], v[34:35], v[34:35], v[60:61]
	v_pk_fma_f32 v[52:53], v[42:43], v[42:43], v[52:53]
	v_pk_fma_f32 v[50:51], v[46:47], v[46:47], v[50:51]
	v_pk_add_f32 v[58:59], v[60:61], v[58:59]
	v_pk_add_f32 v[50:51], v[52:53], v[50:51]
	v_pk_fma_f32 v[4:5], v[36:37], v[36:37], v[4:5]
	v_pk_add_f32 v[50:51], v[58:59], v[50:51]
	v_pk_fma_f32 v[16:17], v[48:49], v[48:49], v[16:17]
	v_add_f32_e32 v73, v50, v51
	s_waitcnt lgkmcnt(2)
	v_mfma_f32_32x32x16_f16 v[50:65], v[54:57], v[102:105], 0
	v_add_f32_e32 v86, v70, v73
	v_sub_f32_e32 v87, v71, v73
	v_sub_f32_e32 v88, v72, v73
	ds_read_b64_tr_b16 v[70:71], v140
	ds_read_b64_tr_b16 v[72:73], v141
	ds_read_b64_tr_b16 v[84:85], v141 offset:32768
	ds_read_b64_tr_b16 v[82:83], v140 offset:32768
	v_pk_fma_f32 v[14:15], v[46:47], v[46:47], v[14:15]
	v_pk_fma_f32 v[12:13], v[44:45], v[44:45], v[12:13]
	v_pk_fma_f32 v[10:11], v[42:43], v[42:43], v[10:11]
	s_waitcnt lgkmcnt(4)
	v_mfma_f32_32x32x16_f16 v[50:65], v[66:69], v[98:101], v[50:65]
	v_fma_f32 v8, v40, v40, v8
	v_fma_f32 v9, v41, v41, v9
	v_fma_f32 v6, v38, v38, v6
	v_fma_f32 v7, v39, v39, v7
	v_fma_f32 v2, v34, v34, v2
	v_fma_f32 v3, v35, v35, v3
	s_nop 5
	v_pk_mul_f32 v[66:67], v[64:65], v[64:65]
	v_pk_mul_f32 v[68:69], v[60:61], v[60:61]
	v_pk_mul_f32 v[74:75], v[56:57], v[56:57]
	v_pk_mul_f32 v[76:77], v[52:53], v[52:53]
	v_pk_fma_f32 v[74:75], v[54:55], v[54:55], v[74:75]
	v_pk_fma_f32 v[76:77], v[50:51], v[50:51], v[76:77]
	v_pk_fma_f32 v[68:69], v[58:59], v[58:59], v[68:69]
	v_pk_fma_f32 v[66:67], v[62:63], v[62:63], v[66:67]
	v_pk_add_f32 v[74:75], v[76:77], v[74:75]
	v_pk_add_f32 v[66:67], v[68:69], v[66:67]
	v_pk_fma_f32 v[4:5], v[52:53], v[52:53], v[4:5]
	v_pk_add_f32 v[66:67], v[74:75], v[66:67]
	v_pk_fma_f32 v[6:7], v[54:55], v[54:55], v[6:7]
	v_add_f32_e32 v89, v66, v67
	s_waitcnt lgkmcnt(2)
	v_mfma_f32_32x32x16_f16 v[66:81], v[70:73], v[102:105], 0
	v_add_f32_e32 v94, v86, v89
	v_add_f32_e32 v126, v87, v89
	v_add_f32_e32 v127, v88, v89
	v_sub_f32_e32 v128, v86, v89
	ds_read_b64_tr_b16 v[86:87], v138
	ds_read_b64_tr_b16 v[88:89], v139
	ds_read_b64_tr_b16 v[124:125], v139 offset:32768
	ds_read_b64_tr_b16 v[122:123], v138 offset:32768
	v_pk_fma_f32 v[8:9], v[56:57], v[56:57], v[8:9]
	v_pk_fma_f32 v[10:11], v[58:59], v[58:59], v[10:11]
	s_waitcnt lgkmcnt(4)
	v_mfma_f32_32x32x16_f16 v[66:81], v[82:85], v[98:101], v[66:81]
	v_fma_f32 v12, v60, v60, v12
	v_fma_f32 v13, v61, v61, v13
	v_fma_f32 v14, v62, v62, v14
	v_fma_f32 v15, v63, v63, v15
	v_fma_f32 v16, v64, v64, v16
	v_fma_f32 v17, v65, v65, v17
	v_pk_fma_f32 v[2:3], v[50:51], v[50:51], v[2:3]
	s_nop 4
	v_pk_mul_f32 v[82:83], v[80:81], v[80:81]
	v_pk_mul_f32 v[84:85], v[76:77], v[76:77]
	v_pk_mul_f32 v[90:91], v[72:73], v[72:73]
	v_pk_mul_f32 v[92:93], v[68:69], v[68:69]
	v_pk_fma_f32 v[90:91], v[70:71], v[70:71], v[90:91]
	v_pk_fma_f32 v[92:93], v[66:67], v[66:67], v[92:93]
	v_pk_fma_f32 v[84:85], v[74:75], v[74:75], v[84:85]
	v_pk_fma_f32 v[82:83], v[78:79], v[78:79], v[82:83]
	v_pk_add_f32 v[90:91], v[92:93], v[90:91]
	v_pk_add_f32 v[82:83], v[84:85], v[82:83]
	v_pk_fma_f32 v[4:5], v[68:69], v[68:69], v[4:5]
	v_pk_add_f32 v[82:83], v[90:91], v[82:83]
	v_pk_fma_f32 v[18:19], v[80:81], v[80:81], v[16:17]
	v_add_f32_e32 v129, v82, v83
	v_add_f32_e32 v131, v94, v129
	s_waitcnt lgkmcnt(2)
	v_mfma_f32_32x32x16_f16 v[82:97], v[86:89], v[102:105], 0
	v_sub_f32_e32 v135, v126, v129
	v_add_f32_e32 v142, v127, v129
	v_sub_f32_e32 v143, v128, v129
	ds_read_b64_tr_b16 v[126:127], v136
	ds_read_b64_tr_b16 v[128:129], v137
	ds_read_b64_tr_b16 v[138:139], v137 offset:32768
	ds_read_b64_tr_b16 v[136:137], v136 offset:32768
	v_pk_fma_f32 v[20:21], v[78:79], v[78:79], v[14:15]
	v_pk_fma_f32 v[22:23], v[76:77], v[76:77], v[12:13]
	v_pk_fma_f32 v[24:25], v[74:75], v[74:75], v[10:11]
	s_waitcnt lgkmcnt(4)
	v_mfma_f32_32x32x16_f16 v[82:97], v[122:125], v[98:101], v[82:97]
	v_fma_f32 v26, v72, v72, v8
	v_fma_f32 v27, v73, v73, v9
	v_fma_f32 v28, v70, v70, v6
	v_fma_f32 v29, v71, v71, v7
	v_fma_f32 v30, v66, v66, v2
	v_fma_f32 v31, v67, v67, v3
	s_nop 5
	v_pk_fma_f32 v[32:33], v[84:85], v[84:85], v[4:5]
	s_waitcnt lgkmcnt(2)
	v_mfma_f32_32x32x16_f16 v[2:17], v[126:129], v[102:105], 0
	v_fma_f32 v28, v86, v86, v28
	v_fma_f32 v29, v87, v87, v29
	v_fma_f32 v24, v90, v90, v24
	v_fma_f32 v25, v91, v91, v25
	v_fma_f32 v22, v92, v92, v22
	v_fma_f32 v23, v93, v93, v23
	v_pk_fma_f32 v[20:21], v[94:95], v[94:95], v[20:21]
	v_pk_fma_f32 v[18:19], v[96:97], v[96:97], v[18:19]
	v_pk_fma_f32 v[30:31], v[82:83], v[82:83], v[30:31]
	v_pk_fma_f32 v[26:27], v[88:89], v[88:89], v[26:27]
	s_waitcnt lgkmcnt(0)
	v_mfma_f32_32x32x16_f16 v[2:17], v[136:139], v[98:101], v[2:17]
	v_mul_f32_e64 v122, v96, v96
	v_mul_f32_e64 v123, v97, v97
	v_mul_f32_e64 v124, v92, v92
	v_mul_f32_e64 v125, v93, v93
	v_mul_f32_e64 v132, v88, v88
	v_mul_f32_e64 v133, v89, v89
	v_pk_mul_f32 v[140:141], v[84:85], v[84:85]
	v_pk_fma_f32 v[132:133], v[86:87], v[86:87], v[132:133]
	v_pk_fma_f32 v[140:141], v[82:83], v[82:83], v[140:141]
	v_pk_fma_f32 v[124:125], v[90:91], v[90:91], v[124:125]
	s_nop 1
	v_pk_mul_f32 v[38:39], v[8:9], v[8:9]
	v_pk_mul_f32 v[40:41], v[4:5], v[4:5]
	v_pk_mul_f32 v[34:35], v[16:17], v[16:17]
	v_pk_mul_f32 v[36:37], v[12:13], v[12:13]
	v_pk_fma_f32 v[16:17], v[16:17], v[16:17], v[18:19]
	v_pk_fma_f32 v[18:19], v[14:15], v[14:15], v[20:21]
	v_pk_fma_f32 v[12:13], v[12:13], v[12:13], v[22:23]
	v_pk_fma_f32 v[20:21], v[10:11], v[10:11], v[24:25]
	v_pk_fma_f32 v[22:23], v[6:7], v[6:7], v[28:29]
	v_pk_fma_f32 v[24:25], v[2:3], v[2:3], v[30:31]
	v_pk_fma_f32 v[2:3], v[2:3], v[2:3], v[40:41]
	v_pk_fma_f32 v[6:7], v[6:7], v[6:7], v[38:39]
	v_pk_fma_f32 v[4:5], v[4:5], v[4:5], v[32:33]
	v_pk_add_f32 v[2:3], v[2:3], v[6:7]
	v_pk_fma_f32 v[6:7], v[10:11], v[10:11], v[36:37]
	v_pk_fma_f32 v[10:11], v[14:15], v[14:15], v[34:35]
	v_pk_fma_f32 v[8:9], v[8:9], v[8:9], v[26:27]
	v_pk_add_f32 v[6:7], v[6:7], v[10:11]
	v_sub_f32_e32 v10, v24, v25
	v_add_f32_e32 v11, v25, v24
	v_add_f32_e32 v10, v4, v10
	v_sub_f32_e32 v14, v11, v4
	v_add_f32_e32 v4, v4, v11
	v_sub_f32_e32 v10, v10, v5
	v_sub_f32_e32 v11, v14, v5
	v_add_f32_e32 v4, v5, v4
	v_add_f32_e32 v5, v22, v10
	v_add_f32_e32 v10, v22, v11
	v_sub_f32_e32 v11, v4, v22
	v_add_f32_e32 v4, v22, v4
	v_sub_f32_e32 v5, v5, v23
	v_add_f32_e32 v10, v23, v10
	v_sub_f32_e32 v11, v11, v23
	v_add_f32_e32 v4, v23, v4
	v_add_f32_e32 v5, v8, v5
	v_sub_f32_e32 v10, v10, v8
	v_sub_f32_e32 v11, v11, v8
	v_add_f32_e32 v4, v8, v4
	v_sub_f32_e32 v5, v5, v9
	v_pk_fma_f32 v[122:123], v[94:95], v[94:95], v[122:123]
	v_sub_f32_e32 v8, v10, v9
	v_sub_f32_e32 v10, v11, v9
	v_add_f32_e32 v4, v9, v4
	v_add_f32_e32 v5, v20, v5
	v_pk_add_f32 v[132:133], v[140:141], v[132:133]
	v_pk_add_f32 v[122:123], v[124:125], v[122:123]
	v_add_f32_e32 v8, v20, v8
	v_add_f32_e32 v9, v20, v10
	v_sub_f32_e32 v4, v4, v20
	v_sub_f32_e32 v5, v5, v21
	v_pk_add_f32 v[122:123], v[132:133], v[122:123]
	v_add_f32_e32 v8, v21, v8
	v_add_f32_e32 v9, v21, v9
	v_sub_f32_e32 v4, v4, v21
	v_add_f32_e32 v5, v12, v5
	v_add_f32_e32 v122, v122, v123
	v_pk_add_f32 v[2:3], v[2:3], v[6:7]
	v_sub_f32_e32 v8, v8, v12
	v_add_f32_e32 v9, v12, v9
	v_sub_f32_e32 v4, v4, v12
	v_sub_f32_e32 v5, v5, v13
	v_add_f32_e32 v123, v131, v122
	v_add_f32_e32 v2, v2, v3
	v_sub_f32_e32 v8, v8, v13
	v_add_f32_e32 v9, v13, v9
	v_sub_f32_e32 v4, v4, v13
	v_add_f32_e32 v5, v18, v5
	v_add_f32_e32 v3, v123, v2
	v_add_f32_e32 v8, v18, v8
	v_sub_f32_e32 v9, v9, v18
	v_sub_f32_e32 v4, v4, v18
	v_sub_f32_e32 v5, v5, v19
	v_and_b32_e32 v10, 8, v156
	v_add_f32_e32 v8, v19, v8
	v_sub_f32_e32 v9, v9, v19
	v_sub_f32_e32 v4, v4, v19
	v_add_f32_e32 v5, v16, v5
	v_cmp_eq_u32_e32 vcc, 0, v10
	v_cndmask_b32_e64 v10, -v3, v3, s[0:1]
	s_cselect_b64 s[0:1], -1, 0
	s_bitcmp0_b32 s4, 7
	v_sub_f32_e32 v8, v8, v16
	v_sub_f32_e32 v9, v9, v16
	v_sub_f32_e32 v4, v4, v16
	v_sub_f32_e32 v5, v5, v17
	v_cndmask_b32_e64 v11, -v3, v3, s[0:1]
	s_cselect_b64 s[0:1], -1, 0
	v_and_b32_e32 v16, 32, v156
	v_sub_f32_e32 v8, v8, v17
	v_cndmask_b32_e64 v5, -v5, v5, vcc
	v_cndmask_b32_e64 v12, -v3, v3, s[0:1]
	v_cndmask_b32_e64 v18, v161, v162, s[2:3]
	v_cmp_eq_u32_e64 s[2:3], 0, v16
	v_lshlrev_b32_e32 v18, 2, v18
	v_cmp_eq_u32_e64 s[0:1], 0, v134
	v_cndmask_b32_e64 v16, v11, v5, s[2:3]
	v_cndmask_b32_e64 v5, v5, v11, s[2:3]
	v_cndmask_b32_e64 v11, v8, v12, s[2:3]
	ds_bpermute_b32 v11, v18, v11
	v_and_b32_e32 v14, 2, v156
	v_cndmask_b32_e64 v13, -v3, v3, s[0:1]
	v_cmp_eq_u32_e64 s[0:1], 0, v14
	v_cndmask_b32_e64 v8, v12, v8, s[2:3]
	v_add_f32_e32 v124, v135, v122
	v_cndmask_b32_e64 v14, -v3, v3, s[0:1]
	v_cmp_eq_u32_e64 s[0:1], 0, v130
	v_sub_f32_e32 v4, v4, v17
	s_waitcnt lgkmcnt(0)
	v_add_f32_e32 v8, v8, v11
	v_cndmask_b32_e64 v15, -v3, v3, s[0:1]
	v_cndmask_b32_e64 v11, v14, v10, s[2:3]
	v_cndmask_b32_e64 v10, v10, v14, s[2:3]
	v_sub_f32_e32 v6, v124, v2
	v_sub_f32_e32 v9, v9, v17
	v_cndmask_b32_e64 v3, -v3, v3, vcc
	ds_bpermute_b32 v10, v18, v10
	v_cndmask_b32_e64 v12, v4, v15, s[2:3]
	v_sub_f32_e32 v125, v142, v122
	v_cndmask_b32_e64 v19, v9, v13, s[2:3]
	v_cndmask_b32_e64 v9, v13, v9, s[2:3]
	ds_bpermute_b32 v12, v18, v12
	v_cndmask_b32_e64 v13, v6, v3, s[2:3]
	v_sub_f32_e32 v7, v125, v2
	v_bfe_i32 v17, v156, 5, 1
	ds_bpermute_b32 v5, v18, v5
	ds_bpermute_b32 v13, v18, v13
	v_sub_f32_e32 v122, v143, v122
	v_cndmask_b32_e64 v3, v3, v6, s[2:3]
	v_and_b32_e32 v6, v17, v7
	v_sub_f32_e32 v2, v122, v2
	ds_bpermute_b32 v19, v18, v19
	ds_bpermute_b32 v6, v18, v6
	s_waitcnt lgkmcnt(5)
	v_add_f32_e32 v10, v11, v10
	v_cndmask_b32_e64 v4, v15, v4, s[2:3]
	v_and_b32_e32 v11, v17, v2
	s_waitcnt lgkmcnt(4)
	v_add_f32_e32 v4, v4, v12
	ds_bpermute_b32 v11, v18, v11
	v_and_b32_e32 v12, 16, v156
	v_cmp_lt_i32_e64 s[4:5], v164, v163
	s_waitcnt lgkmcnt(4)
	v_add_f32_e32 v5, v16, v5
	s_waitcnt lgkmcnt(3)
	v_add_f32_e32 v3, v3, v13
	v_cndmask_b32_e64 v13, v161, v164, s[4:5]
	v_cmp_eq_u32_e64 s[4:5], 0, v12
	s_waitcnt lgkmcnt(2)
	v_add_f32_e32 v9, v9, v19
	v_lshlrev_b32_e32 v13, 2, v13
	v_cndmask_b32_e64 v12, v4, v5, s[4:5]
	v_cndmask_b32_e64 v4, v5, v4, s[4:5]
	v_cndmask_b32_e64 v5, 0, v7, s[2:3]
	s_waitcnt lgkmcnt(1)
	v_add_f32_e32 v5, v5, v6
	v_cndmask_b32_e64 v2, 0, v2, s[2:3]
	v_cndmask_b32_e64 v7, v9, v5, s[4:5]
	ds_bpermute_b32 v4, v13, v4
	s_waitcnt lgkmcnt(1)
	v_add_f32_e32 v2, v2, v11
	v_cndmask_b32_e64 v6, v3, v8, s[4:5]
	v_cndmask_b32_e64 v3, v8, v3, s[4:5]
	ds_bpermute_b32 v7, v13, v7
	ds_bpermute_b32 v3, v13, v3
	v_cndmask_b32_e64 v8, v10, v2, s[4:5]
	ds_bpermute_b32 v8, v13, v8
	v_cndmask_b32_e64 v5, v5, v9, s[4:5]
	s_waitcnt lgkmcnt(3)
	v_add_f32_e32 v4, v12, v4
	s_waitcnt lgkmcnt(2)
	v_add_f32_e32 v5, v5, v7
	s_waitcnt lgkmcnt(1)
	v_add_f32_e32 v3, v6, v3
	v_cndmask_b32_e64 v2, v2, v10, s[4:5]
	v_cndmask_b32_e32 v6, v5, v4, vcc
	v_cndmask_b32_e32 v4, v4, v5, vcc
	v_mov_b32_e32 v5, v155
	s_waitcnt lgkmcnt(0)
	v_add_f32_e32 v2, v2, v8
	v_mov_b32_dpp v5, v4 row_mirror row_mask:0xf bank_mask:0xf
	s_nop 1
	v_add_f32_dpp v4, v5, v6 row_half_mirror row_mask:0xf bank_mask:0xf bound_ctrl:1
	v_cndmask_b32_e32 v5, v2, v3, vcc
	v_cndmask_b32_e32 v2, v3, v2, vcc
	v_mov_b32_e32 v3, v155
	s_nop 1
	v_mov_b32_dpp v3, v2 row_mirror row_mask:0xf bank_mask:0xf
	s_nop 1
	v_add_f32_dpp v2, v3, v5 row_half_mirror row_mask:0xf bank_mask:0xf bound_ctrl:1
	v_cndmask_b32_e64 v3, v2, v4, s[0:1]
	v_cndmask_b32_e64 v2, v4, v2, s[0:1]
	v_mov_b32_e32 v4, v155
	s_nop 1
	v_mov_b32_dpp v4, v2 row_half_mirror row_mask:0xf bank_mask:0xf
	s_nop 1
	v_add_f32_dpp v2, v4, v3 quad_perm:[3,2,1,0] row_mask:0xf bank_mask:0xf bound_ctrl:1
	v_and_b32_e32 v4, 3, v156
	v_cmp_eq_u32_e32 vcc, 0, v4
	v_and_b32_e32 v4, 56, v156
	v_add_f32_dpp v2, v2, v2 quad_perm:[2,3,0,1] row_mask:0xf bank_mask:0xf bound_ctrl:1
	v_mov_b32_e32 v3, 0
	v_cmp_ne_u32_e64 s[0:1], 56, v4
	s_and_b64 s[2:3], vcc, s[0:1]
	v_mov_b32_dpp v3, v2 quad_perm:[1,0,3,2] row_mask:0xf bank_mask:0xf
	s_and_saveexec_b64 s[0:1], s[2:3]
	v_and_b32_e32 v4, 0xfc, v156
	v_add_f32_e32 v2, v2, v3
	v_or_b32_e32 v4, v165, v4
	ds_write_b32 v4, v2
	s_or_b64 exec, exec, s[0:1]
	v_cmp_gt_i32_e32 vcc, 14, v156
	s_waitcnt lgkmcnt(0)
	s_barrier
	s_and_saveexec_b64 s[0:1], vcc
	s_cbranch_execz .LBB1_2
	ds_read_b32 v2, v166
	ds_read_b32 v3, v166 offset:64
	ds_read_b32 v4, v166 offset:128
	ds_read_b32 v5, v166 offset:192
	s_waitcnt lgkmcnt(2)
	v_add_f32_e32 v2, v2, v3
	s_waitcnt lgkmcnt(1)
	v_add_f32_e32 v2, v2, v4
	s_waitcnt lgkmcnt(0)
	v_add_f32_e32 v2, v2, v5
	v_mul_f32_e32 v4, 0x39800000, v2
	v_lshl_add_u64 v[2:3], v[156:157], 2, s[14:15]
	global_store_dword v[2:3], v4, off
	s_branch .LBB1_2
